# hand-written DSA top-256 selection (bit-sliced bisection with in-VGPR half-wave counts via DPP + permlane16_swap, candidate-mask instead of guarded loads, bitop3 bookkeeping)
# speedup vs baseline: 1.0091x; 1.0018x over previous
.LBB0_558:
	v_lshrrev_b32_e32 v1, 5, v245
	s_lshl_b32 s5, s4, 1
	v_and_b32_e32 v0, 31, v146
	v_or_b32_e32 v6, s5, v1
	s_cmpk_gt_i32 s12, 0xc0
	s_mov_b64 s[6:7], -1
	s_waitcnt lgkmcnt(0)
	s_barrier
	s_cbranch_scc0 .LBB0_652
	v_lshl_add_u32 v3, v6, 2, v0
	v_lshlrev_b32_e32 v4, 13, v6
	s_lshr_b32 s12, s18, 5
	s_cmpk_gt_u32 s18, 0x41f
	v_lshl_add_u32 v5, v3, 2, v4
	s_cbranch_scc1 .Lmy_sel2
	ds_read_b32 v76, v5
	ds_read_b32 v77, v5 offset:128
	ds_read_b32 v78, v5 offset:256
	ds_read_b32 v79, v5 offset:384
	ds_read_b32 v80, v5 offset:512
	ds_read_b32 v81, v5 offset:640
	ds_read_b32 v82, v5 offset:768
	ds_read_b32 v83, v5 offset:896
	ds_read_b32 v84, v5 offset:1024
	ds_read_b32 v85, v5 offset:1152
	ds_read_b32 v86, v5 offset:1280
	ds_read_b32 v87, v5 offset:1408
	ds_read_b32 v88, v5 offset:1536
	ds_read_b32 v89, v5 offset:1664
	ds_read_b32 v90, v5 offset:1792
	ds_read_b32 v91, v5 offset:1920
	ds_read_b32 v92, v5 offset:2048
	ds_read_b32 v93, v5 offset:2176
	ds_read_b32 v94, v5 offset:2304
	ds_read_b32 v95, v5 offset:2432
	ds_read_b32 v96, v5 offset:2560
	ds_read_b32 v97, v5 offset:2688
	ds_read_b32 v98, v5 offset:2816
	ds_read_b32 v99, v5 offset:2944
	ds_read_b32 v100, v5 offset:3072
	ds_read_b32 v101, v5 offset:3200
	ds_read_b32 v102, v5 offset:3328
	ds_read_b32 v103, v5 offset:3456
	ds_read_b32 v104, v5 offset:3584
	ds_read_b32 v105, v5 offset:3712
	ds_read_b32 v106, v5 offset:3840
	ds_read_b32 v107, v5 offset:3968
	s_sub_i32 s19, 32, s12
	s_lshl_b32 s19, -1, s19
	v_mov_b32_e32 v10, s19
	v_mov_b32_e32 v12, 0
	v_mov_b32_e32 v14, 0
	v_mov_b32_e32 v15, 0x100
	v_mov_b32_e32 v2, 0
	v_mov_b32_e32 v9, 0
	s_mov_b64 s[40:41], 0
	s_waitcnt lgkmcnt(0)
	s_mov_b32 s12, 0x07060302
	s_mov_b32 s19, 0x05040100
	v_perm_b32 v62, v76, v92, s12
	v_perm_b32 v92, v76, v92, s19
	v_perm_b32 v76, v77, v93, s12
	v_perm_b32 v93, v77, v93, s19
	v_perm_b32 v77, v78, v94, s12
	v_perm_b32 v94, v78, v94, s19
	v_perm_b32 v78, v79, v95, s12
	v_perm_b32 v95, v79, v95, s19
	v_perm_b32 v79, v80, v96, s12
	v_perm_b32 v96, v80, v96, s19
	v_perm_b32 v80, v81, v97, s12
	v_perm_b32 v97, v81, v97, s19
	v_perm_b32 v81, v82, v98, s12
	v_perm_b32 v98, v82, v98, s19
	v_perm_b32 v82, v83, v99, s12
	v_perm_b32 v99, v83, v99, s19
	v_perm_b32 v83, v84, v100, s12
	v_perm_b32 v100, v84, v100, s19
	v_perm_b32 v84, v85, v101, s12
	v_perm_b32 v101, v85, v101, s19
	v_perm_b32 v85, v86, v102, s12
	v_perm_b32 v102, v86, v102, s19
	v_perm_b32 v86, v87, v103, s12
	v_perm_b32 v103, v87, v103, s19
	v_perm_b32 v87, v88, v104, s12
	v_perm_b32 v104, v88, v104, s19
	v_perm_b32 v88, v89, v105, s12
	v_perm_b32 v105, v89, v105, s19
	v_perm_b32 v89, v90, v106, s12
	v_perm_b32 v106, v90, v106, s19
	v_perm_b32 v90, v91, v107, s12
	v_perm_b32 v107, v91, v107, s19
	s_mov_b32 s12, 0x07030501
	s_mov_b32 s19, 0x06020400
	v_perm_b32 v91, v62, v83, s12
	v_perm_b32 v83, v62, v83, s19
	v_perm_b32 v62, v76, v84, s12
	v_perm_b32 v84, v76, v84, s19
	v_perm_b32 v76, v77, v85, s12
	v_perm_b32 v85, v77, v85, s19
	v_perm_b32 v77, v78, v86, s12
	v_perm_b32 v86, v78, v86, s19
	v_perm_b32 v78, v79, v87, s12
	v_perm_b32 v87, v79, v87, s19
	v_perm_b32 v79, v80, v88, s12
	v_perm_b32 v88, v80, v88, s19
	v_perm_b32 v80, v81, v89, s12
	v_perm_b32 v89, v81, v89, s19
	v_perm_b32 v81, v82, v90, s12
	v_perm_b32 v90, v82, v90, s19
	v_perm_b32 v82, v92, v100, s12
	v_perm_b32 v100, v92, v100, s19
	v_perm_b32 v92, v93, v101, s12
	v_perm_b32 v101, v93, v101, s19
	v_perm_b32 v93, v94, v102, s12
	v_perm_b32 v102, v94, v102, s19
	v_perm_b32 v94, v95, v103, s12
	v_perm_b32 v103, v95, v103, s19
	v_perm_b32 v95, v96, v104, s12
	v_perm_b32 v104, v96, v104, s19
	v_perm_b32 v96, v97, v105, s12
	v_perm_b32 v105, v97, v105, s19
	v_perm_b32 v97, v98, v106, s12
	v_perm_b32 v106, v98, v106, s19
	v_perm_b32 v98, v99, v107, s12
	v_perm_b32 v107, v99, v107, s19
	s_mov_b32 s12, 0x0f0f0f0f
	v_lshrrev_b32_e32 v58, 4, v78
	v_lshlrev_b32_e32 v59, 4, v91
	v_bfi_b32 v91, s12, v58, v91
	v_bfi_b32 v78, s12, v78, v59
	v_lshrrev_b32_e32 v60, 4, v79
	v_lshlrev_b32_e32 v61, 4, v62
	v_bfi_b32 v62, s12, v60, v62
	v_bfi_b32 v79, s12, v79, v61
	v_lshrrev_b32_e32 v58, 4, v80
	v_lshlrev_b32_e32 v59, 4, v76
	v_bfi_b32 v76, s12, v58, v76
	v_bfi_b32 v80, s12, v80, v59
	v_lshrrev_b32_e32 v60, 4, v81
	v_lshlrev_b32_e32 v61, 4, v77
	v_bfi_b32 v77, s12, v60, v77
	v_bfi_b32 v81, s12, v81, v61
	v_lshrrev_b32_e32 v58, 4, v87
	v_lshlrev_b32_e32 v59, 4, v83
	v_bfi_b32 v83, s12, v58, v83
	v_bfi_b32 v87, s12, v87, v59
	v_lshrrev_b32_e32 v60, 4, v88
	v_lshlrev_b32_e32 v61, 4, v84
	v_bfi_b32 v84, s12, v60, v84
	v_bfi_b32 v88, s12, v88, v61
	v_lshrrev_b32_e32 v58, 4, v89
	v_lshlrev_b32_e32 v59, 4, v85
	v_bfi_b32 v85, s12, v58, v85
	v_bfi_b32 v89, s12, v89, v59
	v_lshrrev_b32_e32 v60, 4, v90
	v_lshlrev_b32_e32 v61, 4, v86
	v_bfi_b32 v86, s12, v60, v86
	v_bfi_b32 v90, s12, v90, v61
	v_lshrrev_b32_e32 v58, 4, v95
	v_lshlrev_b32_e32 v59, 4, v82
	v_bfi_b32 v82, s12, v58, v82
	v_bfi_b32 v95, s12, v95, v59
	v_lshrrev_b32_e32 v60, 4, v96
	v_lshlrev_b32_e32 v61, 4, v92
	v_bfi_b32 v92, s12, v60, v92
	v_bfi_b32 v96, s12, v96, v61
	v_lshrrev_b32_e32 v58, 4, v97
	v_lshlrev_b32_e32 v59, 4, v93
	v_bfi_b32 v93, s12, v58, v93
	v_bfi_b32 v97, s12, v97, v59
	v_lshrrev_b32_e32 v60, 4, v98
	v_lshlrev_b32_e32 v61, 4, v94
	v_bfi_b32 v94, s12, v60, v94
	v_bfi_b32 v98, s12, v98, v61
	v_lshrrev_b32_e32 v58, 4, v104
	v_lshlrev_b32_e32 v59, 4, v100
	v_bfi_b32 v100, s12, v58, v100
	v_bfi_b32 v104, s12, v104, v59
	v_lshrrev_b32_e32 v60, 4, v105
	v_lshlrev_b32_e32 v61, 4, v101
	v_bfi_b32 v101, s12, v60, v101
	v_bfi_b32 v105, s12, v105, v61
	v_lshrrev_b32_e32 v58, 4, v106
	v_lshlrev_b32_e32 v59, 4, v102
	v_bfi_b32 v102, s12, v58, v102
	v_bfi_b32 v106, s12, v106, v59
	v_lshrrev_b32_e32 v60, 4, v107
	v_lshlrev_b32_e32 v61, 4, v103
	v_bfi_b32 v103, s12, v60, v103
	v_bfi_b32 v107, s12, v107, v61
	s_mov_b32 s12, 0x33333333
	v_lshrrev_b32_e32 v58, 2, v76
	v_lshlrev_b32_e32 v59, 2, v91
	v_bfi_b32 v91, s12, v58, v91
	v_bfi_b32 v76, s12, v76, v59
	v_lshrrev_b32_e32 v60, 2, v77
	v_lshlrev_b32_e32 v61, 2, v62
	v_bfi_b32 v62, s12, v60, v62
	v_bfi_b32 v77, s12, v77, v61
	v_lshrrev_b32_e32 v58, 2, v80
	v_lshlrev_b32_e32 v59, 2, v78
	v_bfi_b32 v78, s12, v58, v78
	v_bfi_b32 v80, s12, v80, v59
	v_lshrrev_b32_e32 v60, 2, v81
	v_lshlrev_b32_e32 v61, 2, v79
	v_bfi_b32 v79, s12, v60, v79
	v_bfi_b32 v81, s12, v81, v61
	v_lshrrev_b32_e32 v58, 2, v85
	v_lshlrev_b32_e32 v59, 2, v83
	v_bfi_b32 v83, s12, v58, v83
	v_bfi_b32 v85, s12, v85, v59
	v_lshrrev_b32_e32 v60, 2, v86
	v_lshlrev_b32_e32 v61, 2, v84
	v_bfi_b32 v84, s12, v60, v84
	v_bfi_b32 v86, s12, v86, v61
	v_lshrrev_b32_e32 v58, 2, v89
	v_lshlrev_b32_e32 v59, 2, v87
	v_bfi_b32 v87, s12, v58, v87
	v_bfi_b32 v89, s12, v89, v59
	v_lshrrev_b32_e32 v60, 2, v90
	v_lshlrev_b32_e32 v61, 2, v88
	v_bfi_b32 v88, s12, v60, v88
	v_bfi_b32 v90, s12, v90, v61
	v_lshrrev_b32_e32 v58, 2, v93
	v_lshlrev_b32_e32 v59, 2, v82
	v_bfi_b32 v82, s12, v58, v82
	v_bfi_b32 v93, s12, v93, v59
	v_lshrrev_b32_e32 v60, 2, v94
	v_lshlrev_b32_e32 v61, 2, v92
	v_bfi_b32 v92, s12, v60, v92
	v_bfi_b32 v94, s12, v94, v61
	v_lshrrev_b32_e32 v58, 2, v97
	v_lshlrev_b32_e32 v59, 2, v95
	v_bfi_b32 v95, s12, v58, v95
	v_bfi_b32 v97, s12, v97, v59
	v_lshrrev_b32_e32 v60, 2, v98
	v_lshlrev_b32_e32 v61, 2, v96
	v_bfi_b32 v96, s12, v60, v96
	v_bfi_b32 v98, s12, v98, v61
	v_lshrrev_b32_e32 v58, 2, v102
	v_lshlrev_b32_e32 v59, 2, v100
	v_bfi_b32 v100, s12, v58, v100
	v_bfi_b32 v102, s12, v102, v59
	v_lshrrev_b32_e32 v60, 2, v103
	v_lshlrev_b32_e32 v61, 2, v101
	v_bfi_b32 v101, s12, v60, v101
	v_bfi_b32 v103, s12, v103, v61
	v_lshrrev_b32_e32 v58, 2, v106
	v_lshlrev_b32_e32 v59, 2, v104
	v_bfi_b32 v104, s12, v58, v104
	v_bfi_b32 v106, s12, v106, v59
	v_lshrrev_b32_e32 v60, 2, v107
	v_lshlrev_b32_e32 v61, 2, v105
	v_bfi_b32 v105, s12, v60, v105
	v_bfi_b32 v107, s12, v107, v61
	s_mov_b32 s12, 0x55555555
	v_lshrrev_b32_e32 v58, 1, v62
	v_lshlrev_b32_e32 v59, 1, v91
	v_bfi_b32 v91, s12, v58, v91
	v_bfi_b32 v62, s12, v62, v59
	v_lshrrev_b32_e32 v60, 1, v77
	v_lshlrev_b32_e32 v61, 1, v76
	v_bfi_b32 v76, s12, v60, v76
	v_bfi_b32 v77, s12, v77, v61
	v_lshrrev_b32_e32 v58, 1, v79
	v_lshlrev_b32_e32 v59, 1, v78
	v_bfi_b32 v78, s12, v58, v78
	v_bfi_b32 v79, s12, v79, v59
	v_lshrrev_b32_e32 v60, 1, v81
	v_lshlrev_b32_e32 v61, 1, v80
	v_bfi_b32 v80, s12, v60, v80
	v_bfi_b32 v81, s12, v81, v61
	v_lshrrev_b32_e32 v58, 1, v84
	v_lshlrev_b32_e32 v59, 1, v83
	v_bfi_b32 v83, s12, v58, v83
	v_bfi_b32 v84, s12, v84, v59
	v_lshrrev_b32_e32 v60, 1, v86
	v_lshlrev_b32_e32 v61, 1, v85
	v_bfi_b32 v85, s12, v60, v85
	v_bfi_b32 v86, s12, v86, v61
	v_lshrrev_b32_e32 v58, 1, v88
	v_lshlrev_b32_e32 v59, 1, v87
	v_bfi_b32 v87, s12, v58, v87
	v_bfi_b32 v88, s12, v88, v59
	v_lshrrev_b32_e32 v60, 1, v90
	v_lshlrev_b32_e32 v61, 1, v89
	v_bfi_b32 v89, s12, v60, v89
	v_bfi_b32 v90, s12, v90, v61
	v_lshrrev_b32_e32 v58, 1, v92
	v_lshlrev_b32_e32 v59, 1, v82
	v_bfi_b32 v82, s12, v58, v82
	v_bfi_b32 v92, s12, v92, v59
	v_lshrrev_b32_e32 v60, 1, v94
	v_lshlrev_b32_e32 v61, 1, v93
	v_bfi_b32 v93, s12, v60, v93
	v_bfi_b32 v94, s12, v94, v61
	v_lshrrev_b32_e32 v58, 1, v96
	v_lshlrev_b32_e32 v59, 1, v95
	v_bfi_b32 v95, s12, v58, v95
	v_bfi_b32 v96, s12, v96, v59
	v_lshrrev_b32_e32 v60, 1, v98
	v_lshlrev_b32_e32 v61, 1, v97
	v_bfi_b32 v97, s12, v60, v97
	v_bfi_b32 v98, s12, v98, v61
	v_lshrrev_b32_e32 v58, 1, v101
	v_lshlrev_b32_e32 v59, 1, v100
	v_bfi_b32 v100, s12, v58, v100
	v_bfi_b32 v101, s12, v101, v59
	v_lshrrev_b32_e32 v60, 1, v103
	v_lshlrev_b32_e32 v61, 1, v102
	v_bfi_b32 v102, s12, v60, v102
	v_bfi_b32 v103, s12, v103, v61
	v_lshrrev_b32_e32 v58, 1, v105
	v_lshlrev_b32_e32 v59, 1, v104
	v_bfi_b32 v104, s12, v58, v104
	v_bfi_b32 v105, s12, v105, v59
	v_lshrrev_b32_e32 v60, 1, v107
	v_lshlrev_b32_e32 v61, 1, v106
	v_bfi_b32 v106, s12, v60, v106
	v_bfi_b32 v107, s12, v107, v61
.Lmy_s1_p0:
	v_and_b32_e32 v50, v10, v91
	v_bcnt_u32_b32 v52, v50, v14
	s_nop 1
	v_add_u32_dpp v53, v52, v52 quad_perm:[1,0,3,2] row_mask:0xf bank_mask:0xf bound_ctrl:1
	s_nop 1
	v_add_u32_dpp v53, v53, v53 quad_perm:[2,3,0,1] row_mask:0xf bank_mask:0xf bound_ctrl:1
	s_nop 1
	v_add_u32_dpp v53, v53, v53 row_half_mirror row_mask:0xf bank_mask:0xf bound_ctrl:1
	s_nop 1
	v_add_u32_dpp v53, v53, v53 row_mirror row_mask:0xf bank_mask:0xf bound_ctrl:1
	v_mov_b32_e32 v54, v53
	s_nop 1
	v_permlane16_swap_b32 v53, v54
	v_add_u32_e32 v53, v53, v54
	v_cmp_gt_i32_e32 vcc, 0x100, v53
	v_cmp_eq_u32_e64 s[8:9], v53, v15
	s_nop 0
	v_cndmask_b32_e64 v55, 0, -1, vcc
	v_cndmask_b32_e32 v14, v14, v52, vcc
	v_bitop3_b32 v12, v12, v50, v55 bitop3:0xf8
	v_bitop3_b32 v10, v10, v91, v55 bitop3:0x60
	s_cmp_lg_u64 s[8:9], 0
	s_cbranch_scc1 .Lmy_s1_h0
.Lmy_s1_p1:
	v_and_b32_e32 v50, v10, v62
	v_bcnt_u32_b32 v52, v50, v14
	s_nop 1
	v_add_u32_dpp v53, v52, v52 quad_perm:[1,0,3,2] row_mask:0xf bank_mask:0xf bound_ctrl:1
	s_nop 1
	v_add_u32_dpp v53, v53, v53 quad_perm:[2,3,0,1] row_mask:0xf bank_mask:0xf bound_ctrl:1
	s_nop 1
	v_add_u32_dpp v53, v53, v53 row_half_mirror row_mask:0xf bank_mask:0xf bound_ctrl:1
	s_nop 1
	v_add_u32_dpp v53, v53, v53 row_mirror row_mask:0xf bank_mask:0xf bound_ctrl:1
	v_mov_b32_e32 v54, v53
	s_nop 1
	v_permlane16_swap_b32 v53, v54
	v_add_u32_e32 v53, v53, v54
	v_cmp_gt_i32_e32 vcc, 0x100, v53
	v_cmp_eq_u32_e64 s[8:9], v53, v15
	s_nop 0
	v_cndmask_b32_e64 v55, 0, -1, vcc
	v_cndmask_b32_e32 v14, v14, v52, vcc
	v_bitop3_b32 v12, v12, v50, v55 bitop3:0xf8
	v_bitop3_b32 v10, v10, v62, v55 bitop3:0x60
	s_cmp_lg_u64 s[8:9], 0
	s_cbranch_scc1 .Lmy_s1_h1
.Lmy_s1_p2:
	v_and_b32_e32 v50, v10, v76
	v_bcnt_u32_b32 v52, v50, v14
	s_nop 1
	v_add_u32_dpp v53, v52, v52 quad_perm:[1,0,3,2] row_mask:0xf bank_mask:0xf bound_ctrl:1
	s_nop 1
	v_add_u32_dpp v53, v53, v53 quad_perm:[2,3,0,1] row_mask:0xf bank_mask:0xf bound_ctrl:1
	s_nop 1
	v_add_u32_dpp v53, v53, v53 row_half_mirror row_mask:0xf bank_mask:0xf bound_ctrl:1
	s_nop 1
	v_add_u32_dpp v53, v53, v53 row_mirror row_mask:0xf bank_mask:0xf bound_ctrl:1
	v_mov_b32_e32 v54, v53
	s_nop 1
	v_permlane16_swap_b32 v53, v54
	v_add_u32_e32 v53, v53, v54
	v_cmp_gt_i32_e32 vcc, 0x100, v53
	v_cmp_eq_u32_e64 s[8:9], v53, v15
	s_nop 0
	v_cndmask_b32_e64 v55, 0, -1, vcc
	v_cndmask_b32_e32 v14, v14, v52, vcc
	v_bitop3_b32 v12, v12, v50, v55 bitop3:0xf8
	v_bitop3_b32 v10, v10, v76, v55 bitop3:0x60
	s_cmp_lg_u64 s[8:9], 0
	s_cbranch_scc1 .Lmy_s1_h2
.Lmy_s1_p3:
	v_and_b32_e32 v50, v10, v77
	v_bcnt_u32_b32 v52, v50, v14
	s_nop 1
	v_add_u32_dpp v53, v52, v52 quad_perm:[1,0,3,2] row_mask:0xf bank_mask:0xf bound_ctrl:1
	s_nop 1
	v_add_u32_dpp v53, v53, v53 quad_perm:[2,3,0,1] row_mask:0xf bank_mask:0xf bound_ctrl:1
	s_nop 1
	v_add_u32_dpp v53, v53, v53 row_half_mirror row_mask:0xf bank_mask:0xf bound_ctrl:1
	s_nop 1
	v_add_u32_dpp v53, v53, v53 row_mirror row_mask:0xf bank_mask:0xf bound_ctrl:1
	v_mov_b32_e32 v54, v53
	s_nop 1
	v_permlane16_swap_b32 v53, v54
	v_add_u32_e32 v53, v53, v54
	v_cmp_gt_i32_e32 vcc, 0x100, v53
	v_cmp_eq_u32_e64 s[8:9], v53, v15
	s_nop 0
	v_cndmask_b32_e64 v55, 0, -1, vcc
	v_cndmask_b32_e32 v14, v14, v52, vcc
	v_bitop3_b32 v12, v12, v50, v55 bitop3:0xf8
	v_bitop3_b32 v10, v10, v77, v55 bitop3:0x60
	s_cmp_lg_u64 s[8:9], 0
	s_cbranch_scc1 .Lmy_s1_h3
.Lmy_s1_p4:
	v_and_b32_e32 v50, v10, v78
	v_bcnt_u32_b32 v52, v50, v14
	s_nop 1
	v_add_u32_dpp v53, v52, v52 quad_perm:[1,0,3,2] row_mask:0xf bank_mask:0xf bound_ctrl:1
	s_nop 1
	v_add_u32_dpp v53, v53, v53 quad_perm:[2,3,0,1] row_mask:0xf bank_mask:0xf bound_ctrl:1
	s_nop 1
	v_add_u32_dpp v53, v53, v53 row_half_mirror row_mask:0xf bank_mask:0xf bound_ctrl:1
	s_nop 1
	v_add_u32_dpp v53, v53, v53 row_mirror row_mask:0xf bank_mask:0xf bound_ctrl:1
	v_mov_b32_e32 v54, v53
	s_nop 1
	v_permlane16_swap_b32 v53, v54
	v_add_u32_e32 v53, v53, v54
	v_cmp_gt_i32_e32 vcc, 0x100, v53
	v_cmp_eq_u32_e64 s[8:9], v53, v15
	s_nop 0
	v_cndmask_b32_e64 v55, 0, -1, vcc
	v_cndmask_b32_e32 v14, v14, v52, vcc
	v_bitop3_b32 v12, v12, v50, v55 bitop3:0xf8
	v_bitop3_b32 v10, v10, v78, v55 bitop3:0x60
	s_cmp_lg_u64 s[8:9], 0
	s_cbranch_scc1 .Lmy_s1_h4
.Lmy_s1_p5:
	v_and_b32_e32 v50, v10, v79
	v_bcnt_u32_b32 v52, v50, v14
	s_nop 1
	v_add_u32_dpp v53, v52, v52 quad_perm:[1,0,3,2] row_mask:0xf bank_mask:0xf bound_ctrl:1
	s_nop 1
	v_add_u32_dpp v53, v53, v53 quad_perm:[2,3,0,1] row_mask:0xf bank_mask:0xf bound_ctrl:1
	s_nop 1
	v_add_u32_dpp v53, v53, v53 row_half_mirror row_mask:0xf bank_mask:0xf bound_ctrl:1
	s_nop 1
	v_add_u32_dpp v53, v53, v53 row_mirror row_mask:0xf bank_mask:0xf bound_ctrl:1
	v_mov_b32_e32 v54, v53
	s_nop 1
	v_permlane16_swap_b32 v53, v54
	v_add_u32_e32 v53, v53, v54
	v_cmp_gt_i32_e32 vcc, 0x100, v53
	v_cmp_eq_u32_e64 s[8:9], v53, v15
	s_nop 0
	v_cndmask_b32_e64 v55, 0, -1, vcc
	v_cndmask_b32_e32 v14, v14, v52, vcc
	v_bitop3_b32 v12, v12, v50, v55 bitop3:0xf8
	v_bitop3_b32 v10, v10, v79, v55 bitop3:0x60
	s_cmp_lg_u64 s[8:9], 0
	s_cbranch_scc1 .Lmy_s1_h5
.Lmy_s1_p6:
	v_and_b32_e32 v50, v10, v80
	v_bcnt_u32_b32 v52, v50, v14
	s_nop 1
	v_add_u32_dpp v53, v52, v52 quad_perm:[1,0,3,2] row_mask:0xf bank_mask:0xf bound_ctrl:1
	s_nop 1
	v_add_u32_dpp v53, v53, v53 quad_perm:[2,3,0,1] row_mask:0xf bank_mask:0xf bound_ctrl:1
	s_nop 1
	v_add_u32_dpp v53, v53, v53 row_half_mirror row_mask:0xf bank_mask:0xf bound_ctrl:1
	s_nop 1
	v_add_u32_dpp v53, v53, v53 row_mirror row_mask:0xf bank_mask:0xf bound_ctrl:1
	v_mov_b32_e32 v54, v53
	s_nop 1
	v_permlane16_swap_b32 v53, v54
	v_add_u32_e32 v53, v53, v54
	v_cmp_gt_i32_e32 vcc, 0x100, v53
	v_cmp_eq_u32_e64 s[8:9], v53, v15
	s_nop 0
	v_cndmask_b32_e64 v55, 0, -1, vcc
	v_cndmask_b32_e32 v14, v14, v52, vcc
	v_bitop3_b32 v12, v12, v50, v55 bitop3:0xf8
	v_bitop3_b32 v10, v10, v80, v55 bitop3:0x60
	s_cmp_lg_u64 s[8:9], 0
	s_cbranch_scc1 .Lmy_s1_h6
.Lmy_s1_p7:
	v_and_b32_e32 v50, v10, v81
	v_bcnt_u32_b32 v52, v50, v14
	s_nop 1
	v_add_u32_dpp v53, v52, v52 quad_perm:[1,0,3,2] row_mask:0xf bank_mask:0xf bound_ctrl:1
	s_nop 1
	v_add_u32_dpp v53, v53, v53 quad_perm:[2,3,0,1] row_mask:0xf bank_mask:0xf bound_ctrl:1
	s_nop 1
	v_add_u32_dpp v53, v53, v53 row_half_mirror row_mask:0xf bank_mask:0xf bound_ctrl:1
	s_nop 1
	v_add_u32_dpp v53, v53, v53 row_mirror row_mask:0xf bank_mask:0xf bound_ctrl:1
	v_mov_b32_e32 v54, v53
	s_nop 1
	v_permlane16_swap_b32 v53, v54
	v_add_u32_e32 v53, v53, v54
	v_cmp_gt_i32_e32 vcc, 0x100, v53
	v_cmp_eq_u32_e64 s[8:9], v53, v15
	s_nop 0
	v_cndmask_b32_e64 v55, 0, -1, vcc
	v_cndmask_b32_e32 v14, v14, v52, vcc
	v_bitop3_b32 v12, v12, v50, v55 bitop3:0xf8
	v_bitop3_b32 v10, v10, v81, v55 bitop3:0x60
	s_cmp_lg_u64 s[8:9], 0
	s_cbranch_scc1 .Lmy_s1_h7
.Lmy_s1_p8:
	v_and_b32_e32 v50, v10, v83
	v_bcnt_u32_b32 v52, v50, v14
	s_nop 1
	v_add_u32_dpp v53, v52, v52 quad_perm:[1,0,3,2] row_mask:0xf bank_mask:0xf bound_ctrl:1
	s_nop 1
	v_add_u32_dpp v53, v53, v53 quad_perm:[2,3,0,1] row_mask:0xf bank_mask:0xf bound_ctrl:1
	s_nop 1
	v_add_u32_dpp v53, v53, v53 row_half_mirror row_mask:0xf bank_mask:0xf bound_ctrl:1
	s_nop 1
	v_add_u32_dpp v53, v53, v53 row_mirror row_mask:0xf bank_mask:0xf bound_ctrl:1
	v_mov_b32_e32 v54, v53
	s_nop 1
	v_permlane16_swap_b32 v53, v54
	v_add_u32_e32 v53, v53, v54
	v_cmp_gt_i32_e32 vcc, 0x100, v53
	v_cmp_eq_u32_e64 s[8:9], v53, v15
	s_nop 0
	v_cndmask_b32_e64 v55, 0, -1, vcc
	v_cndmask_b32_e32 v14, v14, v52, vcc
	v_bitop3_b32 v12, v12, v50, v55 bitop3:0xf8
	v_bitop3_b32 v10, v10, v83, v55 bitop3:0x60
	s_cmp_lg_u64 s[8:9], 0
	s_cbranch_scc1 .Lmy_s1_h8
.Lmy_s1_p9:
	v_and_b32_e32 v50, v10, v84
	v_bcnt_u32_b32 v52, v50, v14
	s_nop 1
	v_add_u32_dpp v53, v52, v52 quad_perm:[1,0,3,2] row_mask:0xf bank_mask:0xf bound_ctrl:1
	s_nop 1
	v_add_u32_dpp v53, v53, v53 quad_perm:[2,3,0,1] row_mask:0xf bank_mask:0xf bound_ctrl:1
	s_nop 1
	v_add_u32_dpp v53, v53, v53 row_half_mirror row_mask:0xf bank_mask:0xf bound_ctrl:1
	s_nop 1
	v_add_u32_dpp v53, v53, v53 row_mirror row_mask:0xf bank_mask:0xf bound_ctrl:1
	v_mov_b32_e32 v54, v53
	s_nop 1
	v_permlane16_swap_b32 v53, v54
	v_add_u32_e32 v53, v53, v54
	v_cmp_gt_i32_e32 vcc, 0x100, v53
	v_cmp_eq_u32_e64 s[8:9], v53, v15
	s_nop 0
	v_cndmask_b32_e64 v55, 0, -1, vcc
	v_cndmask_b32_e32 v14, v14, v52, vcc
	v_bitop3_b32 v12, v12, v50, v55 bitop3:0xf8
	v_bitop3_b32 v10, v10, v84, v55 bitop3:0x60
	s_cmp_lg_u64 s[8:9], 0
	s_cbranch_scc1 .Lmy_s1_h9
.Lmy_s1_p10:
	v_and_b32_e32 v50, v10, v85
	v_bcnt_u32_b32 v52, v50, v14
	s_nop 1
	v_add_u32_dpp v53, v52, v52 quad_perm:[1,0,3,2] row_mask:0xf bank_mask:0xf bound_ctrl:1
	s_nop 1
	v_add_u32_dpp v53, v53, v53 quad_perm:[2,3,0,1] row_mask:0xf bank_mask:0xf bound_ctrl:1
	s_nop 1
	v_add_u32_dpp v53, v53, v53 row_half_mirror row_mask:0xf bank_mask:0xf bound_ctrl:1
	s_nop 1
	v_add_u32_dpp v53, v53, v53 row_mirror row_mask:0xf bank_mask:0xf bound_ctrl:1
	v_mov_b32_e32 v54, v53
	s_nop 1
	v_permlane16_swap_b32 v53, v54
	v_add_u32_e32 v53, v53, v54
	v_cmp_gt_i32_e32 vcc, 0x100, v53
	v_cmp_eq_u32_e64 s[8:9], v53, v15
	s_nop 0
	v_cndmask_b32_e64 v55, 0, -1, vcc
	v_cndmask_b32_e32 v14, v14, v52, vcc
	v_bitop3_b32 v12, v12, v50, v55 bitop3:0xf8
	v_bitop3_b32 v10, v10, v85, v55 bitop3:0x60
	s_cmp_lg_u64 s[8:9], 0
	s_cbranch_scc1 .Lmy_s1_h10
.Lmy_s1_p11:
	v_and_b32_e32 v50, v10, v86
	v_bcnt_u32_b32 v52, v50, v14
	s_nop 1
	v_add_u32_dpp v53, v52, v52 quad_perm:[1,0,3,2] row_mask:0xf bank_mask:0xf bound_ctrl:1
	s_nop 1
	v_add_u32_dpp v53, v53, v53 quad_perm:[2,3,0,1] row_mask:0xf bank_mask:0xf bound_ctrl:1
	s_nop 1
	v_add_u32_dpp v53, v53, v53 row_half_mirror row_mask:0xf bank_mask:0xf bound_ctrl:1
	s_nop 1
	v_add_u32_dpp v53, v53, v53 row_mirror row_mask:0xf bank_mask:0xf bound_ctrl:1
	v_mov_b32_e32 v54, v53
	s_nop 1
	v_permlane16_swap_b32 v53, v54
	v_add_u32_e32 v53, v53, v54
	v_cmp_gt_i32_e32 vcc, 0x100, v53
	v_cmp_eq_u32_e64 s[8:9], v53, v15
	s_nop 0
	v_cndmask_b32_e64 v55, 0, -1, vcc
	v_cndmask_b32_e32 v14, v14, v52, vcc
	v_bitop3_b32 v12, v12, v50, v55 bitop3:0xf8
	v_bitop3_b32 v10, v10, v86, v55 bitop3:0x60
	s_cmp_lg_u64 s[8:9], 0
	s_cbranch_scc1 .Lmy_s1_h11
.Lmy_s1_p12:
	v_and_b32_e32 v50, v10, v87
	v_bcnt_u32_b32 v52, v50, v14
	s_nop 1
	v_add_u32_dpp v53, v52, v52 quad_perm:[1,0,3,2] row_mask:0xf bank_mask:0xf bound_ctrl:1
	s_nop 1
	v_add_u32_dpp v53, v53, v53 quad_perm:[2,3,0,1] row_mask:0xf bank_mask:0xf bound_ctrl:1
	s_nop 1
	v_add_u32_dpp v53, v53, v53 row_half_mirror row_mask:0xf bank_mask:0xf bound_ctrl:1
	s_nop 1
	v_add_u32_dpp v53, v53, v53 row_mirror row_mask:0xf bank_mask:0xf bound_ctrl:1
	v_mov_b32_e32 v54, v53
	s_nop 1
	v_permlane16_swap_b32 v53, v54
	v_add_u32_e32 v53, v53, v54
	v_cmp_gt_i32_e32 vcc, 0x100, v53
	v_cmp_eq_u32_e64 s[8:9], v53, v15
	s_nop 0
	v_cndmask_b32_e64 v55, 0, -1, vcc
	v_cndmask_b32_e32 v14, v14, v52, vcc
	v_bitop3_b32 v12, v12, v50, v55 bitop3:0xf8
	v_bitop3_b32 v10, v10, v87, v55 bitop3:0x60
	s_cmp_lg_u64 s[8:9], 0
	s_cbranch_scc1 .Lmy_s1_h12
.Lmy_s1_p13:
	v_and_b32_e32 v50, v10, v88
	v_bcnt_u32_b32 v52, v50, v14
	s_nop 1
	v_add_u32_dpp v53, v52, v52 quad_perm:[1,0,3,2] row_mask:0xf bank_mask:0xf bound_ctrl:1
	s_nop 1
	v_add_u32_dpp v53, v53, v53 quad_perm:[2,3,0,1] row_mask:0xf bank_mask:0xf bound_ctrl:1
	s_nop 1
	v_add_u32_dpp v53, v53, v53 row_half_mirror row_mask:0xf bank_mask:0xf bound_ctrl:1
	s_nop 1
	v_add_u32_dpp v53, v53, v53 row_mirror row_mask:0xf bank_mask:0xf bound_ctrl:1
	v_mov_b32_e32 v54, v53
	s_nop 1
	v_permlane16_swap_b32 v53, v54
	v_add_u32_e32 v53, v53, v54
	v_cmp_gt_i32_e32 vcc, 0x100, v53
	v_cmp_eq_u32_e64 s[8:9], v53, v15
	s_nop 0
	v_cndmask_b32_e64 v55, 0, -1, vcc
	v_cndmask_b32_e32 v14, v14, v52, vcc
	v_bitop3_b32 v12, v12, v50, v55 bitop3:0xf8
	v_bitop3_b32 v10, v10, v88, v55 bitop3:0x60
	s_cmp_lg_u64 s[8:9], 0
	s_cbranch_scc1 .Lmy_s1_h13
.Lmy_s1_p14:
	v_and_b32_e32 v50, v10, v89
	v_bcnt_u32_b32 v52, v50, v14
	s_nop 1
	v_add_u32_dpp v53, v52, v52 quad_perm:[1,0,3,2] row_mask:0xf bank_mask:0xf bound_ctrl:1
	s_nop 1
	v_add_u32_dpp v53, v53, v53 quad_perm:[2,3,0,1] row_mask:0xf bank_mask:0xf bound_ctrl:1
	s_nop 1
	v_add_u32_dpp v53, v53, v53 row_half_mirror row_mask:0xf bank_mask:0xf bound_ctrl:1
	s_nop 1
	v_add_u32_dpp v53, v53, v53 row_mirror row_mask:0xf bank_mask:0xf bound_ctrl:1
	v_mov_b32_e32 v54, v53
	s_nop 1
	v_permlane16_swap_b32 v53, v54
	v_add_u32_e32 v53, v53, v54
	v_cmp_gt_i32_e32 vcc, 0x100, v53
	v_cmp_eq_u32_e64 s[8:9], v53, v15
	s_nop 0
	v_cndmask_b32_e64 v55, 0, -1, vcc
	v_cndmask_b32_e32 v14, v14, v52, vcc
	v_bitop3_b32 v12, v12, v50, v55 bitop3:0xf8
	v_bitop3_b32 v10, v10, v89, v55 bitop3:0x60
	s_cmp_lg_u64 s[8:9], 0
	s_cbranch_scc1 .Lmy_s1_h14
.Lmy_s1_p15:
	v_and_b32_e32 v50, v10, v90
	v_bcnt_u32_b32 v52, v50, v14
	s_nop 1
	v_add_u32_dpp v53, v52, v52 quad_perm:[1,0,3,2] row_mask:0xf bank_mask:0xf bound_ctrl:1
	s_nop 1
	v_add_u32_dpp v53, v53, v53 quad_perm:[2,3,0,1] row_mask:0xf bank_mask:0xf bound_ctrl:1
	s_nop 1
	v_add_u32_dpp v53, v53, v53 row_half_mirror row_mask:0xf bank_mask:0xf bound_ctrl:1
	s_nop 1
	v_add_u32_dpp v53, v53, v53 row_mirror row_mask:0xf bank_mask:0xf bound_ctrl:1
	v_mov_b32_e32 v54, v53
	s_nop 1
	v_permlane16_swap_b32 v53, v54
	v_add_u32_e32 v53, v53, v54
	v_cmp_gt_i32_e32 vcc, 0x100, v53
	v_cmp_eq_u32_e64 s[8:9], v53, v15
	s_nop 0
	v_cndmask_b32_e64 v55, 0, -1, vcc
	v_cndmask_b32_e32 v14, v14, v52, vcc
	v_bitop3_b32 v12, v12, v50, v55 bitop3:0xf8
	v_bitop3_b32 v10, v10, v90, v55 bitop3:0x60
	s_cmp_lg_u64 s[8:9], 0
	s_cbranch_scc1 .Lmy_s1_h15
.Lmy_s1_p16:
	v_and_b32_e32 v50, v10, v82
	v_bcnt_u32_b32 v52, v50, v14
	s_nop 1
	v_add_u32_dpp v53, v52, v52 quad_perm:[1,0,3,2] row_mask:0xf bank_mask:0xf bound_ctrl:1
	s_nop 1
	v_add_u32_dpp v53, v53, v53 quad_perm:[2,3,0,1] row_mask:0xf bank_mask:0xf bound_ctrl:1
	s_nop 1
	v_add_u32_dpp v53, v53, v53 row_half_mirror row_mask:0xf bank_mask:0xf bound_ctrl:1
	s_nop 1
	v_add_u32_dpp v53, v53, v53 row_mirror row_mask:0xf bank_mask:0xf bound_ctrl:1
	v_mov_b32_e32 v54, v53
	s_nop 1
	v_permlane16_swap_b32 v53, v54
	v_add_u32_e32 v53, v53, v54
	v_cmp_gt_i32_e32 vcc, 0x100, v53
	v_cmp_eq_u32_e64 s[8:9], v53, v15
	s_nop 0
	v_cndmask_b32_e64 v55, 0, -1, vcc
	v_cndmask_b32_e32 v14, v14, v52, vcc
	v_bitop3_b32 v12, v12, v50, v55 bitop3:0xf8
	v_bitop3_b32 v10, v10, v82, v55 bitop3:0x60
	s_cmp_lg_u64 s[8:9], 0
	s_cbranch_scc1 .Lmy_s1_h16
.Lmy_s1_p17:
	v_and_b32_e32 v50, v10, v92
	v_bcnt_u32_b32 v52, v50, v14
	s_nop 1
	v_add_u32_dpp v53, v52, v52 quad_perm:[1,0,3,2] row_mask:0xf bank_mask:0xf bound_ctrl:1
	s_nop 1
	v_add_u32_dpp v53, v53, v53 quad_perm:[2,3,0,1] row_mask:0xf bank_mask:0xf bound_ctrl:1
	s_nop 1
	v_add_u32_dpp v53, v53, v53 row_half_mirror row_mask:0xf bank_mask:0xf bound_ctrl:1
	s_nop 1
	v_add_u32_dpp v53, v53, v53 row_mirror row_mask:0xf bank_mask:0xf bound_ctrl:1
	v_mov_b32_e32 v54, v53
	s_nop 1
	v_permlane16_swap_b32 v53, v54
	v_add_u32_e32 v53, v53, v54
	v_cmp_gt_i32_e32 vcc, 0x100, v53
	v_cmp_eq_u32_e64 s[8:9], v53, v15
	s_nop 0
	v_cndmask_b32_e64 v55, 0, -1, vcc
	v_cndmask_b32_e32 v14, v14, v52, vcc
	v_bitop3_b32 v12, v12, v50, v55 bitop3:0xf8
	v_bitop3_b32 v10, v10, v92, v55 bitop3:0x60
	s_cmp_lg_u64 s[8:9], 0
	s_cbranch_scc1 .Lmy_s1_h17
.Lmy_s1_p18:
	v_and_b32_e32 v50, v10, v93
	v_bcnt_u32_b32 v52, v50, v14
	s_nop 1
	v_add_u32_dpp v53, v52, v52 quad_perm:[1,0,3,2] row_mask:0xf bank_mask:0xf bound_ctrl:1
	s_nop 1
	v_add_u32_dpp v53, v53, v53 quad_perm:[2,3,0,1] row_mask:0xf bank_mask:0xf bound_ctrl:1
	s_nop 1
	v_add_u32_dpp v53, v53, v53 row_half_mirror row_mask:0xf bank_mask:0xf bound_ctrl:1
	s_nop 1
	v_add_u32_dpp v53, v53, v53 row_mirror row_mask:0xf bank_mask:0xf bound_ctrl:1
	v_mov_b32_e32 v54, v53
	s_nop 1
	v_permlane16_swap_b32 v53, v54
	v_add_u32_e32 v53, v53, v54
	v_cmp_gt_i32_e32 vcc, 0x100, v53
	v_cmp_eq_u32_e64 s[8:9], v53, v15
	s_nop 0
	v_cndmask_b32_e64 v55, 0, -1, vcc
	v_cndmask_b32_e32 v14, v14, v52, vcc
	v_bitop3_b32 v12, v12, v50, v55 bitop3:0xf8
	v_bitop3_b32 v10, v10, v93, v55 bitop3:0x60
	s_cmp_lg_u64 s[8:9], 0
	s_cbranch_scc1 .Lmy_s1_h18
.Lmy_s1_p19:
	v_and_b32_e32 v50, v10, v94
	v_bcnt_u32_b32 v52, v50, v14
	s_nop 1
	v_add_u32_dpp v53, v52, v52 quad_perm:[1,0,3,2] row_mask:0xf bank_mask:0xf bound_ctrl:1
	s_nop 1
	v_add_u32_dpp v53, v53, v53 quad_perm:[2,3,0,1] row_mask:0xf bank_mask:0xf bound_ctrl:1
	s_nop 1
	v_add_u32_dpp v53, v53, v53 row_half_mirror row_mask:0xf bank_mask:0xf bound_ctrl:1
	s_nop 1
	v_add_u32_dpp v53, v53, v53 row_mirror row_mask:0xf bank_mask:0xf bound_ctrl:1
	v_mov_b32_e32 v54, v53
	s_nop 1
	v_permlane16_swap_b32 v53, v54
	v_add_u32_e32 v53, v53, v54
	v_cmp_gt_i32_e32 vcc, 0x100, v53
	v_cmp_eq_u32_e64 s[8:9], v53, v15
	s_nop 0
	v_cndmask_b32_e64 v55, 0, -1, vcc
	v_cndmask_b32_e32 v14, v14, v52, vcc
	v_bitop3_b32 v12, v12, v50, v55 bitop3:0xf8
	v_bitop3_b32 v10, v10, v94, v55 bitop3:0x60
	s_cmp_lg_u64 s[8:9], 0
	s_cbranch_scc1 .Lmy_s1_h19
.Lmy_s1_p20:
	v_and_b32_e32 v50, v10, v95
	v_bcnt_u32_b32 v52, v50, v14
	s_nop 1
	v_add_u32_dpp v53, v52, v52 quad_perm:[1,0,3,2] row_mask:0xf bank_mask:0xf bound_ctrl:1
	s_nop 1
	v_add_u32_dpp v53, v53, v53 quad_perm:[2,3,0,1] row_mask:0xf bank_mask:0xf bound_ctrl:1
	s_nop 1
	v_add_u32_dpp v53, v53, v53 row_half_mirror row_mask:0xf bank_mask:0xf bound_ctrl:1
	s_nop 1
	v_add_u32_dpp v53, v53, v53 row_mirror row_mask:0xf bank_mask:0xf bound_ctrl:1
	v_mov_b32_e32 v54, v53
	s_nop 1
	v_permlane16_swap_b32 v53, v54
	v_add_u32_e32 v53, v53, v54
	v_cmp_gt_i32_e32 vcc, 0x100, v53
	v_cmp_eq_u32_e64 s[8:9], v53, v15
	s_nop 0
	v_cndmask_b32_e64 v55, 0, -1, vcc
	v_cndmask_b32_e32 v14, v14, v52, vcc
	v_bitop3_b32 v12, v12, v50, v55 bitop3:0xf8
	v_bitop3_b32 v10, v10, v95, v55 bitop3:0x60
	s_cmp_lg_u64 s[8:9], 0
	s_cbranch_scc1 .Lmy_s1_h20
.Lmy_s1_p21:
	v_and_b32_e32 v50, v10, v96
	v_bcnt_u32_b32 v52, v50, v14
	s_nop 1
	v_add_u32_dpp v53, v52, v52 quad_perm:[1,0,3,2] row_mask:0xf bank_mask:0xf bound_ctrl:1
	s_nop 1
	v_add_u32_dpp v53, v53, v53 quad_perm:[2,3,0,1] row_mask:0xf bank_mask:0xf bound_ctrl:1
	s_nop 1
	v_add_u32_dpp v53, v53, v53 row_half_mirror row_mask:0xf bank_mask:0xf bound_ctrl:1
	s_nop 1
	v_add_u32_dpp v53, v53, v53 row_mirror row_mask:0xf bank_mask:0xf bound_ctrl:1
	v_mov_b32_e32 v54, v53
	s_nop 1
	v_permlane16_swap_b32 v53, v54
	v_add_u32_e32 v53, v53, v54
	v_cmp_gt_i32_e32 vcc, 0x100, v53
	v_cmp_eq_u32_e64 s[8:9], v53, v15
	s_nop 0
	v_cndmask_b32_e64 v55, 0, -1, vcc
	v_cndmask_b32_e32 v14, v14, v52, vcc
	v_bitop3_b32 v12, v12, v50, v55 bitop3:0xf8
	v_bitop3_b32 v10, v10, v96, v55 bitop3:0x60
	s_cmp_lg_u64 s[8:9], 0
	s_cbranch_scc1 .Lmy_s1_h21
.Lmy_s1_p22:
	v_and_b32_e32 v50, v10, v97
	v_bcnt_u32_b32 v52, v50, v14
	s_nop 1
	v_add_u32_dpp v53, v52, v52 quad_perm:[1,0,3,2] row_mask:0xf bank_mask:0xf bound_ctrl:1
	s_nop 1
	v_add_u32_dpp v53, v53, v53 quad_perm:[2,3,0,1] row_mask:0xf bank_mask:0xf bound_ctrl:1
	s_nop 1
	v_add_u32_dpp v53, v53, v53 row_half_mirror row_mask:0xf bank_mask:0xf bound_ctrl:1
	s_nop 1
	v_add_u32_dpp v53, v53, v53 row_mirror row_mask:0xf bank_mask:0xf bound_ctrl:1
	v_mov_b32_e32 v54, v53
	s_nop 1
	v_permlane16_swap_b32 v53, v54
	v_add_u32_e32 v53, v53, v54
	v_cmp_gt_i32_e32 vcc, 0x100, v53
	v_cmp_eq_u32_e64 s[8:9], v53, v15
	s_nop 0
	v_cndmask_b32_e64 v55, 0, -1, vcc
	v_cndmask_b32_e32 v14, v14, v52, vcc
	v_bitop3_b32 v12, v12, v50, v55 bitop3:0xf8
	v_bitop3_b32 v10, v10, v97, v55 bitop3:0x60
	s_cmp_lg_u64 s[8:9], 0
	s_cbranch_scc1 .Lmy_s1_h22
.Lmy_s1_p23:
	v_and_b32_e32 v50, v10, v98
	v_bcnt_u32_b32 v52, v50, v14
	s_nop 1
	v_add_u32_dpp v53, v52, v52 quad_perm:[1,0,3,2] row_mask:0xf bank_mask:0xf bound_ctrl:1
	s_nop 1
	v_add_u32_dpp v53, v53, v53 quad_perm:[2,3,0,1] row_mask:0xf bank_mask:0xf bound_ctrl:1
	s_nop 1
	v_add_u32_dpp v53, v53, v53 row_half_mirror row_mask:0xf bank_mask:0xf bound_ctrl:1
	s_nop 1
	v_add_u32_dpp v53, v53, v53 row_mirror row_mask:0xf bank_mask:0xf bound_ctrl:1
	v_mov_b32_e32 v54, v53
	s_nop 1
	v_permlane16_swap_b32 v53, v54
	v_add_u32_e32 v53, v53, v54
	v_cmp_gt_i32_e32 vcc, 0x100, v53
	v_cmp_eq_u32_e64 s[8:9], v53, v15
	s_nop 0
	v_cndmask_b32_e64 v55, 0, -1, vcc
	v_cndmask_b32_e32 v14, v14, v52, vcc
	v_bitop3_b32 v12, v12, v50, v55 bitop3:0xf8
	v_bitop3_b32 v10, v10, v98, v55 bitop3:0x60
	s_cmp_lg_u64 s[8:9], 0
	s_cbranch_scc1 .Lmy_s1_h23
.Lmy_s1_p24:
	v_and_b32_e32 v50, v10, v100
	v_bcnt_u32_b32 v52, v50, v14
	s_nop 1
	v_add_u32_dpp v53, v52, v52 quad_perm:[1,0,3,2] row_mask:0xf bank_mask:0xf bound_ctrl:1
	s_nop 1
	v_add_u32_dpp v53, v53, v53 quad_perm:[2,3,0,1] row_mask:0xf bank_mask:0xf bound_ctrl:1
	s_nop 1
	v_add_u32_dpp v53, v53, v53 row_half_mirror row_mask:0xf bank_mask:0xf bound_ctrl:1
	s_nop 1
	v_add_u32_dpp v53, v53, v53 row_mirror row_mask:0xf bank_mask:0xf bound_ctrl:1
	v_mov_b32_e32 v54, v53
	s_nop 1
	v_permlane16_swap_b32 v53, v54
	v_add_u32_e32 v53, v53, v54
	v_cmp_gt_i32_e32 vcc, 0x100, v53
	v_cmp_eq_u32_e64 s[8:9], v53, v15
	s_nop 0
	v_cndmask_b32_e64 v55, 0, -1, vcc
	v_cndmask_b32_e32 v14, v14, v52, vcc
	v_bitop3_b32 v12, v12, v50, v55 bitop3:0xf8
	v_bitop3_b32 v10, v10, v100, v55 bitop3:0x60
	s_cmp_lg_u64 s[8:9], 0
	s_cbranch_scc1 .Lmy_s1_h24
.Lmy_s1_p25:
	v_and_b32_e32 v50, v10, v101
	v_bcnt_u32_b32 v52, v50, v14
	s_nop 1
	v_add_u32_dpp v53, v52, v52 quad_perm:[1,0,3,2] row_mask:0xf bank_mask:0xf bound_ctrl:1
	s_nop 1
	v_add_u32_dpp v53, v53, v53 quad_perm:[2,3,0,1] row_mask:0xf bank_mask:0xf bound_ctrl:1
	s_nop 1
	v_add_u32_dpp v53, v53, v53 row_half_mirror row_mask:0xf bank_mask:0xf bound_ctrl:1
	s_nop 1
	v_add_u32_dpp v53, v53, v53 row_mirror row_mask:0xf bank_mask:0xf bound_ctrl:1
	v_mov_b32_e32 v54, v53
	s_nop 1
	v_permlane16_swap_b32 v53, v54
	v_add_u32_e32 v53, v53, v54
	v_cmp_gt_i32_e32 vcc, 0x100, v53
	v_cmp_eq_u32_e64 s[8:9], v53, v15
	s_nop 0
	v_cndmask_b32_e64 v55, 0, -1, vcc
	v_cndmask_b32_e32 v14, v14, v52, vcc
	v_bitop3_b32 v12, v12, v50, v55 bitop3:0xf8
	v_bitop3_b32 v10, v10, v101, v55 bitop3:0x60
	s_cmp_lg_u64 s[8:9], 0
	s_cbranch_scc1 .Lmy_s1_h25
.Lmy_s1_p26:
	v_and_b32_e32 v50, v10, v102
	v_bcnt_u32_b32 v52, v50, v14
	s_nop 1
	v_add_u32_dpp v53, v52, v52 quad_perm:[1,0,3,2] row_mask:0xf bank_mask:0xf bound_ctrl:1
	s_nop 1
	v_add_u32_dpp v53, v53, v53 quad_perm:[2,3,0,1] row_mask:0xf bank_mask:0xf bound_ctrl:1
	s_nop 1
	v_add_u32_dpp v53, v53, v53 row_half_mirror row_mask:0xf bank_mask:0xf bound_ctrl:1
	s_nop 1
	v_add_u32_dpp v53, v53, v53 row_mirror row_mask:0xf bank_mask:0xf bound_ctrl:1
	v_mov_b32_e32 v54, v53
	s_nop 1
	v_permlane16_swap_b32 v53, v54
	v_add_u32_e32 v53, v53, v54
	v_cmp_gt_i32_e32 vcc, 0x100, v53
	v_cmp_eq_u32_e64 s[8:9], v53, v15
	s_nop 0
	v_cndmask_b32_e64 v55, 0, -1, vcc
	v_cndmask_b32_e32 v14, v14, v52, vcc
	v_bitop3_b32 v12, v12, v50, v55 bitop3:0xf8
	v_bitop3_b32 v10, v10, v102, v55 bitop3:0x60
	s_cmp_lg_u64 s[8:9], 0
	s_cbranch_scc1 .Lmy_s1_h26
.Lmy_s1_p27:
	v_and_b32_e32 v50, v10, v103
	v_bcnt_u32_b32 v52, v50, v14
	s_nop 1
	v_add_u32_dpp v53, v52, v52 quad_perm:[1,0,3,2] row_mask:0xf bank_mask:0xf bound_ctrl:1
	s_nop 1
	v_add_u32_dpp v53, v53, v53 quad_perm:[2,3,0,1] row_mask:0xf bank_mask:0xf bound_ctrl:1
	s_nop 1
	v_add_u32_dpp v53, v53, v53 row_half_mirror row_mask:0xf bank_mask:0xf bound_ctrl:1
	s_nop 1
	v_add_u32_dpp v53, v53, v53 row_mirror row_mask:0xf bank_mask:0xf bound_ctrl:1
	v_mov_b32_e32 v54, v53
	s_nop 1
	v_permlane16_swap_b32 v53, v54
	v_add_u32_e32 v53, v53, v54
	v_cmp_gt_i32_e32 vcc, 0x100, v53
	v_cmp_eq_u32_e64 s[8:9], v53, v15
	s_nop 0
	v_cndmask_b32_e64 v55, 0, -1, vcc
	v_cndmask_b32_e32 v14, v14, v52, vcc
	v_bitop3_b32 v12, v12, v50, v55 bitop3:0xf8
	v_bitop3_b32 v10, v10, v103, v55 bitop3:0x60
	s_cmp_lg_u64 s[8:9], 0
	s_cbranch_scc1 .Lmy_s1_h27
.Lmy_s1_p28:
	v_and_b32_e32 v50, v10, v104
	v_bcnt_u32_b32 v52, v50, v14
	s_nop 1
	v_add_u32_dpp v53, v52, v52 quad_perm:[1,0,3,2] row_mask:0xf bank_mask:0xf bound_ctrl:1
	s_nop 1
	v_add_u32_dpp v53, v53, v53 quad_perm:[2,3,0,1] row_mask:0xf bank_mask:0xf bound_ctrl:1
	s_nop 1
	v_add_u32_dpp v53, v53, v53 row_half_mirror row_mask:0xf bank_mask:0xf bound_ctrl:1
	s_nop 1
	v_add_u32_dpp v53, v53, v53 row_mirror row_mask:0xf bank_mask:0xf bound_ctrl:1
	v_mov_b32_e32 v54, v53
	s_nop 1
	v_permlane16_swap_b32 v53, v54
	v_add_u32_e32 v53, v53, v54
	v_cmp_gt_i32_e32 vcc, 0x100, v53
	v_cmp_eq_u32_e64 s[8:9], v53, v15
	s_nop 0
	v_cndmask_b32_e64 v55, 0, -1, vcc
	v_cndmask_b32_e32 v14, v14, v52, vcc
	v_bitop3_b32 v12, v12, v50, v55 bitop3:0xf8
	v_bitop3_b32 v10, v10, v104, v55 bitop3:0x60
	s_cmp_lg_u64 s[8:9], 0
	s_cbranch_scc1 .Lmy_s1_h28
.Lmy_s1_p29:
	v_and_b32_e32 v50, v10, v105
	v_bcnt_u32_b32 v52, v50, v14
	s_nop 1
	v_add_u32_dpp v53, v52, v52 quad_perm:[1,0,3,2] row_mask:0xf bank_mask:0xf bound_ctrl:1
	s_nop 1
	v_add_u32_dpp v53, v53, v53 quad_perm:[2,3,0,1] row_mask:0xf bank_mask:0xf bound_ctrl:1
	s_nop 1
	v_add_u32_dpp v53, v53, v53 row_half_mirror row_mask:0xf bank_mask:0xf bound_ctrl:1
	s_nop 1
	v_add_u32_dpp v53, v53, v53 row_mirror row_mask:0xf bank_mask:0xf bound_ctrl:1
	v_mov_b32_e32 v54, v53
	s_nop 1
	v_permlane16_swap_b32 v53, v54
	v_add_u32_e32 v53, v53, v54
	v_cmp_gt_i32_e32 vcc, 0x100, v53
	v_cmp_eq_u32_e64 s[8:9], v53, v15
	s_nop 0
	v_cndmask_b32_e64 v55, 0, -1, vcc
	v_cndmask_b32_e32 v14, v14, v52, vcc
	v_bitop3_b32 v12, v12, v50, v55 bitop3:0xf8
	v_bitop3_b32 v10, v10, v105, v55 bitop3:0x60
	s_cmp_lg_u64 s[8:9], 0
	s_cbranch_scc1 .Lmy_s1_h29
.Lmy_s1_p30:
	v_and_b32_e32 v50, v10, v106
	v_bcnt_u32_b32 v52, v50, v14
	s_nop 1
	v_add_u32_dpp v53, v52, v52 quad_perm:[1,0,3,2] row_mask:0xf bank_mask:0xf bound_ctrl:1
	s_nop 1
	v_add_u32_dpp v53, v53, v53 quad_perm:[2,3,0,1] row_mask:0xf bank_mask:0xf bound_ctrl:1
	s_nop 1
	v_add_u32_dpp v53, v53, v53 row_half_mirror row_mask:0xf bank_mask:0xf bound_ctrl:1
	s_nop 1
	v_add_u32_dpp v53, v53, v53 row_mirror row_mask:0xf bank_mask:0xf bound_ctrl:1
	v_mov_b32_e32 v54, v53
	s_nop 1
	v_permlane16_swap_b32 v53, v54
	v_add_u32_e32 v53, v53, v54
	v_cmp_gt_i32_e32 vcc, 0x100, v53
	v_cmp_eq_u32_e64 s[8:9], v53, v15
	s_nop 0
	v_cndmask_b32_e64 v55, 0, -1, vcc
	v_cndmask_b32_e32 v14, v14, v52, vcc
	v_bitop3_b32 v12, v12, v50, v55 bitop3:0xf8
	v_bitop3_b32 v10, v10, v106, v55 bitop3:0x60
	s_cmp_lg_u64 s[8:9], 0
	s_cbranch_scc1 .Lmy_s1_h30
.Lmy_s1_p31:
	v_and_b32_e32 v50, v10, v107
	v_bcnt_u32_b32 v52, v50, v14
	s_nop 1
	v_add_u32_dpp v53, v52, v52 quad_perm:[1,0,3,2] row_mask:0xf bank_mask:0xf bound_ctrl:1
	s_nop 1
	v_add_u32_dpp v53, v53, v53 quad_perm:[2,3,0,1] row_mask:0xf bank_mask:0xf bound_ctrl:1
	s_nop 1
	v_add_u32_dpp v53, v53, v53 row_half_mirror row_mask:0xf bank_mask:0xf bound_ctrl:1
	s_nop 1
	v_add_u32_dpp v53, v53, v53 row_mirror row_mask:0xf bank_mask:0xf bound_ctrl:1
	v_mov_b32_e32 v54, v53
	s_nop 1
	v_permlane16_swap_b32 v53, v54
	v_add_u32_e32 v53, v53, v54
	v_cmp_gt_i32_e32 vcc, 0x100, v53
	v_cmp_eq_u32_e64 s[8:9], v53, v15
	s_nop 0
	v_cndmask_b32_e64 v55, 0, -1, vcc
	v_cndmask_b32_e32 v14, v14, v52, vcc
	v_bitop3_b32 v12, v12, v50, v55 bitop3:0xf8
	v_bitop3_b32 v10, v10, v107, v55 bitop3:0x60
	s_cmp_lg_u64 s[8:9], 0
	s_cbranch_scc1 .Lmy_s1_h31
.Lmy_s1_tie:
	s_nop 1
	v_add_u32_dpp v53, v14, v14 quad_perm:[1,0,3,2] row_mask:0xf bank_mask:0xf bound_ctrl:1
	s_nop 1
	v_add_u32_dpp v53, v53, v53 quad_perm:[2,3,0,1] row_mask:0xf bank_mask:0xf bound_ctrl:1
	s_nop 1
	v_add_u32_dpp v53, v53, v53 row_half_mirror row_mask:0xf bank_mask:0xf bound_ctrl:1
	s_nop 1
	v_add_u32_dpp v53, v53, v53 row_mirror row_mask:0xf bank_mask:0xf bound_ctrl:1
	v_mov_b32_e32 v54, v53
	s_nop 1
	v_permlane16_swap_b32 v53, v54
	v_add_u32_e32 v53, v53, v54
	v_sub_u32_e32 v16, 0x100, v53
	v_bcnt_u32_b32 v17, v10, 0
	v_mov_b32_e32 v18, v17
	s_nop 1
	v_add_u32_dpp v19, v18, v18 row_shr:1 row_mask:0xf bank_mask:0xf bound_ctrl:1
	s_nop 1
	v_add_u32_dpp v19, v19, v19 row_shr:2 row_mask:0xf bank_mask:0xf bound_ctrl:1
	s_nop 1
	v_add_u32_dpp v19, v19, v19 row_shr:4 row_mask:0xf bank_mask:0xf bound_ctrl:1
	s_nop 1
	v_add_u32_dpp v19, v19, v19 row_shr:8 row_mask:0xf bank_mask:0xf bound_ctrl:1
	v_mov_b32_e32 v20, 0
	s_nop 1
	v_mov_b32_dpp v20, v19 row_bcast:15 row_mask:0xa bank_mask:0xf
	v_add_u32_e32 v19, v19, v20
	v_sub_u32_e32 v19, v19, v18
	v_sub_u32_e32 v21, v16, v19
	v_max_i32_e32 v21, 0, v21
	v_min_i32_e32 v21, v21, v18
	v_cndmask_b32_e64 v21, v21, 0, s[40:41]
	v_min_i32_e32 v22, v21, v17
	v_sub_u32_e32 v23, v21, v22
	v_mov_b32_e32 v24, 0
	v_mov_b32_e32 v25, 0
	s_mov_b64 s[44:45], exec
.Lmy_s1_tb0:
	v_cmp_lt_i32_e32 vcc, 0, v22
	s_and_b64 exec, exec, vcc
	s_cbranch_execz .Lmy_s1_tbe0
	v_ffbh_u32_e32 v26, v10
	v_lshrrev_b32_e64 v26, v26, s30
	v_or_b32_e32 v24, v24, v26
	v_xor_b32_e32 v10, v10, v26
	v_add_u32_e32 v22, -1, v22
	s_branch .Lmy_s1_tb0
.Lmy_s1_tbe0:
	s_mov_b64 exec, s[44:45]
	v_or_b32_e32 v24, v12, v24
	v_cndmask_b32_e64 v2, v24, v2, s[40:41]

.Lmy_s1_h0:
	s_andn2_b64 s[8:9], s[8:9], s[40:41]
	v_or_b32_e32 v56, v12, v10
	s_or_b64 s[40:41], s[40:41], s[8:9]
	v_cndmask_b32_e64 v2, v2, v56, s[8:9]
	s_cmp_eq_u64 s[40:41], -1
	s_cbranch_scc1 .Lmy_s1_done
	s_branch .Lmy_s1_p1

.Lmy_sel2:
	ds_read_b32 v76, v5
	ds_read_b32 v77, v5 offset:128
	ds_read_b32 v78, v5 offset:256
	ds_read_b32 v79, v5 offset:384
	ds_read_b32 v80, v5 offset:512
	ds_read_b32 v81, v5 offset:640
	ds_read_b32 v82, v5 offset:768
	ds_read_b32 v83, v5 offset:896
	ds_read_b32 v84, v5 offset:1024
	ds_read_b32 v85, v5 offset:1152
	ds_read_b32 v86, v5 offset:1280
	ds_read_b32 v87, v5 offset:1408
	ds_read_b32 v88, v5 offset:1536
	ds_read_b32 v89, v5 offset:1664
	ds_read_b32 v90, v5 offset:1792
	ds_read_b32 v91, v5 offset:1920
	ds_read_b32 v92, v5 offset:2048
	ds_read_b32 v93, v5 offset:2176
	ds_read_b32 v94, v5 offset:2304
	ds_read_b32 v95, v5 offset:2432
	ds_read_b32 v96, v5 offset:2560
	ds_read_b32 v97, v5 offset:2688
	ds_read_b32 v98, v5 offset:2816
	ds_read_b32 v99, v5 offset:2944
	ds_read_b32 v100, v5 offset:3072
	ds_read_b32 v101, v5 offset:3200
	ds_read_b32 v102, v5 offset:3328
	ds_read_b32 v103, v5 offset:3456
	ds_read_b32 v104, v5 offset:3584
	ds_read_b32 v105, v5 offset:3712
	ds_read_b32 v106, v5 offset:3840
	ds_read_b32 v107, v5 offset:3968
	ds_read_b32 v108, v5 offset:4096
	ds_read_b32 v109, v5 offset:4224
	ds_read_b32 v110, v5 offset:4352
	ds_read_b32 v111, v5 offset:4480
	ds_read_b32 v112, v5 offset:4608
	ds_read_b32 v113, v5 offset:4736
	ds_read_b32 v114, v5 offset:4864
	ds_read_b32 v115, v5 offset:4992
	ds_read_b32 v116, v5 offset:5120
	ds_read_b32 v117, v5 offset:5248
	ds_read_b32 v118, v5 offset:5376
	ds_read_b32 v119, v5 offset:5504
	ds_read_b32 v120, v5 offset:5632
	ds_read_b32 v121, v5 offset:5760
	ds_read_b32 v122, v5 offset:5888
	ds_read_b32 v123, v5 offset:6016
	ds_read_b32 v124, v5 offset:6144
	ds_read_b32 v125, v5 offset:6272
	ds_read_b32 v126, v5 offset:6400
	ds_read_b32 v127, v5 offset:6528
	ds_read_b32 v128, v5 offset:6656
	ds_read_b32 v129, v5 offset:6784
	ds_read_b32 v130, v5 offset:6912
	ds_read_b32 v131, v5 offset:7040
	ds_read_b32 v132, v5 offset:7168
	ds_read_b32 v133, v5 offset:7296
	ds_read_b32 v134, v5 offset:7424
	ds_read_b32 v135, v5 offset:7552
	ds_read_b32 v136, v5 offset:7680
	ds_read_b32 v137, v5 offset:7808
	v_add_u32_e32 v58, 0x7c0, v3
	v_and_b32_e32 v58, 0x7ff, v58
	v_lshl_add_u32 v58, v58, 2, v4
	ds_read_b32 v138, v58
	v_add_u32_e32 v59, 0x7e0, v3
	v_and_b32_e32 v59, 0x7ff, v59
	v_lshl_add_u32 v59, v59, 2, v4
	ds_read_b32 v139, v59
	s_sub_i32 s19, 64, s12
	s_lshl_b32 s19, -1, s19
	v_mov_b32_e32 v10, -1
	v_mov_b32_e32 v11, s19
	v_mov_b32_e32 v12, 0
	v_mov_b32_e32 v13, 0
	v_mov_b32_e32 v14, 0
	v_mov_b32_e32 v15, 0x100
	v_mov_b32_e32 v2, 0
	v_mov_b32_e32 v9, 0
	s_mov_b64 s[40:41], 0
	s_waitcnt lgkmcnt(0)
	s_mov_b32 s12, 0x07060302
	s_mov_b32 s19, 0x05040100
	v_perm_b32 v62, v76, v92, s12
	v_perm_b32 v92, v76, v92, s19
	v_perm_b32 v76, v77, v93, s12
	v_perm_b32 v93, v77, v93, s19
	v_perm_b32 v77, v78, v94, s12
	v_perm_b32 v94, v78, v94, s19
	v_perm_b32 v78, v79, v95, s12
	v_perm_b32 v95, v79, v95, s19
	v_perm_b32 v79, v80, v96, s12
	v_perm_b32 v96, v80, v96, s19
	v_perm_b32 v80, v81, v97, s12
	v_perm_b32 v97, v81, v97, s19
	v_perm_b32 v81, v82, v98, s12
	v_perm_b32 v98, v82, v98, s19
	v_perm_b32 v82, v83, v99, s12
	v_perm_b32 v99, v83, v99, s19
	v_perm_b32 v83, v84, v100, s12
	v_perm_b32 v100, v84, v100, s19
	v_perm_b32 v84, v85, v101, s12
	v_perm_b32 v101, v85, v101, s19
	v_perm_b32 v85, v86, v102, s12
	v_perm_b32 v102, v86, v102, s19
	v_perm_b32 v86, v87, v103, s12
	v_perm_b32 v103, v87, v103, s19
	v_perm_b32 v87, v88, v104, s12
	v_perm_b32 v104, v88, v104, s19
	v_perm_b32 v88, v89, v105, s12
	v_perm_b32 v105, v89, v105, s19
	v_perm_b32 v89, v90, v106, s12
	v_perm_b32 v106, v90, v106, s19
	v_perm_b32 v90, v91, v107, s12
	v_perm_b32 v107, v91, v107, s19
	s_mov_b32 s12, 0x07030501
	s_mov_b32 s19, 0x06020400
	v_perm_b32 v91, v62, v83, s12
	v_perm_b32 v83, v62, v83, s19
	v_perm_b32 v62, v76, v84, s12
	v_perm_b32 v84, v76, v84, s19
	v_perm_b32 v76, v77, v85, s12
	v_perm_b32 v85, v77, v85, s19
	v_perm_b32 v77, v78, v86, s12
	v_perm_b32 v86, v78, v86, s19
	v_perm_b32 v78, v79, v87, s12
	v_perm_b32 v87, v79, v87, s19
	v_perm_b32 v79, v80, v88, s12
	v_perm_b32 v88, v80, v88, s19
	v_perm_b32 v80, v81, v89, s12
	v_perm_b32 v89, v81, v89, s19
	v_perm_b32 v81, v82, v90, s12
	v_perm_b32 v90, v82, v90, s19
	v_perm_b32 v82, v92, v100, s12
	v_perm_b32 v100, v92, v100, s19
	v_perm_b32 v92, v93, v101, s12
	v_perm_b32 v101, v93, v101, s19
	v_perm_b32 v93, v94, v102, s12
	v_perm_b32 v102, v94, v102, s19
	v_perm_b32 v94, v95, v103, s12
	v_perm_b32 v103, v95, v103, s19
	v_perm_b32 v95, v96, v104, s12
	v_perm_b32 v104, v96, v104, s19
	v_perm_b32 v96, v97, v105, s12
	v_perm_b32 v105, v97, v105, s19
	v_perm_b32 v97, v98, v106, s12
	v_perm_b32 v106, v98, v106, s19
	v_perm_b32 v98, v99, v107, s12
	v_perm_b32 v107, v99, v107, s19
	s_mov_b32 s12, 0x0f0f0f0f
	v_lshrrev_b32_e32 v58, 4, v78
	v_lshlrev_b32_e32 v59, 4, v91
	v_bfi_b32 v91, s12, v58, v91
	v_bfi_b32 v78, s12, v78, v59
	v_lshrrev_b32_e32 v60, 4, v79
	v_lshlrev_b32_e32 v61, 4, v62
	v_bfi_b32 v62, s12, v60, v62
	v_bfi_b32 v79, s12, v79, v61
	v_lshrrev_b32_e32 v58, 4, v80
	v_lshlrev_b32_e32 v59, 4, v76
	v_bfi_b32 v76, s12, v58, v76
	v_bfi_b32 v80, s12, v80, v59
	v_lshrrev_b32_e32 v60, 4, v81
	v_lshlrev_b32_e32 v61, 4, v77
	v_bfi_b32 v77, s12, v60, v77
	v_bfi_b32 v81, s12, v81, v61
	v_lshrrev_b32_e32 v58, 4, v87
	v_lshlrev_b32_e32 v59, 4, v83
	v_bfi_b32 v83, s12, v58, v83
	v_bfi_b32 v87, s12, v87, v59
	v_lshrrev_b32_e32 v60, 4, v88
	v_lshlrev_b32_e32 v61, 4, v84
	v_bfi_b32 v84, s12, v60, v84
	v_bfi_b32 v88, s12, v88, v61
	v_lshrrev_b32_e32 v58, 4, v89
	v_lshlrev_b32_e32 v59, 4, v85
	v_bfi_b32 v85, s12, v58, v85
	v_bfi_b32 v89, s12, v89, v59
	v_lshrrev_b32_e32 v60, 4, v90
	v_lshlrev_b32_e32 v61, 4, v86
	v_bfi_b32 v86, s12, v60, v86
	v_bfi_b32 v90, s12, v90, v61
	v_lshrrev_b32_e32 v58, 4, v95
	v_lshlrev_b32_e32 v59, 4, v82
	v_bfi_b32 v82, s12, v58, v82
	v_bfi_b32 v95, s12, v95, v59
	v_lshrrev_b32_e32 v60, 4, v96
	v_lshlrev_b32_e32 v61, 4, v92
	v_bfi_b32 v92, s12, v60, v92
	v_bfi_b32 v96, s12, v96, v61
	v_lshrrev_b32_e32 v58, 4, v97
	v_lshlrev_b32_e32 v59, 4, v93
	v_bfi_b32 v93, s12, v58, v93
	v_bfi_b32 v97, s12, v97, v59
	v_lshrrev_b32_e32 v60, 4, v98
	v_lshlrev_b32_e32 v61, 4, v94
	v_bfi_b32 v94, s12, v60, v94
	v_bfi_b32 v98, s12, v98, v61
	v_lshrrev_b32_e32 v58, 4, v104
	v_lshlrev_b32_e32 v59, 4, v100
	v_bfi_b32 v100, s12, v58, v100
	v_bfi_b32 v104, s12, v104, v59
	v_lshrrev_b32_e32 v60, 4, v105
	v_lshlrev_b32_e32 v61, 4, v101
	v_bfi_b32 v101, s12, v60, v101
	v_bfi_b32 v105, s12, v105, v61
	v_lshrrev_b32_e32 v58, 4, v106
	v_lshlrev_b32_e32 v59, 4, v102
	v_bfi_b32 v102, s12, v58, v102
	v_bfi_b32 v106, s12, v106, v59
	v_lshrrev_b32_e32 v60, 4, v107
	v_lshlrev_b32_e32 v61, 4, v103
	v_bfi_b32 v103, s12, v60, v103
	v_bfi_b32 v107, s12, v107, v61
	s_mov_b32 s12, 0x33333333
	v_lshrrev_b32_e32 v58, 2, v76
	v_lshlrev_b32_e32 v59, 2, v91
	v_bfi_b32 v91, s12, v58, v91
	v_bfi_b32 v76, s12, v76, v59
	v_lshrrev_b32_e32 v60, 2, v77
	v_lshlrev_b32_e32 v61, 2, v62
	v_bfi_b32 v62, s12, v60, v62
	v_bfi_b32 v77, s12, v77, v61
	v_lshrrev_b32_e32 v58, 2, v80
	v_lshlrev_b32_e32 v59, 2, v78
	v_bfi_b32 v78, s12, v58, v78
	v_bfi_b32 v80, s12, v80, v59
	v_lshrrev_b32_e32 v60, 2, v81
	v_lshlrev_b32_e32 v61, 2, v79
	v_bfi_b32 v79, s12, v60, v79
	v_bfi_b32 v81, s12, v81, v61
	v_lshrrev_b32_e32 v58, 2, v85
	v_lshlrev_b32_e32 v59, 2, v83
	v_bfi_b32 v83, s12, v58, v83
	v_bfi_b32 v85, s12, v85, v59
	v_lshrrev_b32_e32 v60, 2, v86
	v_lshlrev_b32_e32 v61, 2, v84
	v_bfi_b32 v84, s12, v60, v84
	v_bfi_b32 v86, s12, v86, v61
	v_lshrrev_b32_e32 v58, 2, v89
	v_lshlrev_b32_e32 v59, 2, v87
	v_bfi_b32 v87, s12, v58, v87
	v_bfi_b32 v89, s12, v89, v59
	v_lshrrev_b32_e32 v60, 2, v90
	v_lshlrev_b32_e32 v61, 2, v88
	v_bfi_b32 v88, s12, v60, v88
	v_bfi_b32 v90, s12, v90, v61
	v_lshrrev_b32_e32 v58, 2, v93
	v_lshlrev_b32_e32 v59, 2, v82
	v_bfi_b32 v82, s12, v58, v82
	v_bfi_b32 v93, s12, v93, v59
	v_lshrrev_b32_e32 v60, 2, v94
	v_lshlrev_b32_e32 v61, 2, v92
	v_bfi_b32 v92, s12, v60, v92
	v_bfi_b32 v94, s12, v94, v61
	v_lshrrev_b32_e32 v58, 2, v97
	v_lshlrev_b32_e32 v59, 2, v95
	v_bfi_b32 v95, s12, v58, v95
	v_bfi_b32 v97, s12, v97, v59
	v_lshrrev_b32_e32 v60, 2, v98
	v_lshlrev_b32_e32 v61, 2, v96
	v_bfi_b32 v96, s12, v60, v96
	v_bfi_b32 v98, s12, v98, v61
	v_lshrrev_b32_e32 v58, 2, v102
	v_lshlrev_b32_e32 v59, 2, v100
	v_bfi_b32 v100, s12, v58, v100
	v_bfi_b32 v102, s12, v102, v59
	v_lshrrev_b32_e32 v60, 2, v103
	v_lshlrev_b32_e32 v61, 2, v101
	v_bfi_b32 v101, s12, v60, v101
	v_bfi_b32 v103, s12, v103, v61
	v_lshrrev_b32_e32 v58, 2, v106
	v_lshlrev_b32_e32 v59, 2, v104
	v_bfi_b32 v104, s12, v58, v104
	v_bfi_b32 v106, s12, v106, v59
	v_lshrrev_b32_e32 v60, 2, v107
	v_lshlrev_b32_e32 v61, 2, v105
	v_bfi_b32 v105, s12, v60, v105
	v_bfi_b32 v107, s12, v107, v61
	s_mov_b32 s12, 0x55555555
	v_lshrrev_b32_e32 v58, 1, v62
	v_lshlrev_b32_e32 v59, 1, v91
	v_bfi_b32 v91, s12, v58, v91
	v_bfi_b32 v62, s12, v62, v59
	v_lshrrev_b32_e32 v60, 1, v77
	v_lshlrev_b32_e32 v61, 1, v76
	v_bfi_b32 v76, s12, v60, v76
	v_bfi_b32 v77, s12, v77, v61
	v_lshrrev_b32_e32 v58, 1, v79
	v_lshlrev_b32_e32 v59, 1, v78
	v_bfi_b32 v78, s12, v58, v78
	v_bfi_b32 v79, s12, v79, v59
	v_lshrrev_b32_e32 v60, 1, v81
	v_lshlrev_b32_e32 v61, 1, v80
	v_bfi_b32 v80, s12, v60, v80
	v_bfi_b32 v81, s12, v81, v61
	v_lshrrev_b32_e32 v58, 1, v84
	v_lshlrev_b32_e32 v59, 1, v83
	v_bfi_b32 v83, s12, v58, v83
	v_bfi_b32 v84, s12, v84, v59
	v_lshrrev_b32_e32 v60, 1, v86
	v_lshlrev_b32_e32 v61, 1, v85
	v_bfi_b32 v85, s12, v60, v85
	v_bfi_b32 v86, s12, v86, v61
	v_lshrrev_b32_e32 v58, 1, v88
	v_lshlrev_b32_e32 v59, 1, v87
	v_bfi_b32 v87, s12, v58, v87
	v_bfi_b32 v88, s12, v88, v59
	v_lshrrev_b32_e32 v60, 1, v90
	v_lshlrev_b32_e32 v61, 1, v89
	v_bfi_b32 v89, s12, v60, v89
	v_bfi_b32 v90, s12, v90, v61
	v_lshrrev_b32_e32 v58, 1, v92
	v_lshlrev_b32_e32 v59, 1, v82
	v_bfi_b32 v82, s12, v58, v82
	v_bfi_b32 v92, s12, v92, v59
	v_lshrrev_b32_e32 v60, 1, v94
	v_lshlrev_b32_e32 v61, 1, v93
	v_bfi_b32 v93, s12, v60, v93
	v_bfi_b32 v94, s12, v94, v61
	v_lshrrev_b32_e32 v58, 1, v96
	v_lshlrev_b32_e32 v59, 1, v95
	v_bfi_b32 v95, s12, v58, v95
	v_bfi_b32 v96, s12, v96, v59
	v_lshrrev_b32_e32 v60, 1, v98
	v_lshlrev_b32_e32 v61, 1, v97
	v_bfi_b32 v97, s12, v60, v97
	v_bfi_b32 v98, s12, v98, v61
	v_lshrrev_b32_e32 v58, 1, v101
	v_lshlrev_b32_e32 v59, 1, v100
	v_bfi_b32 v100, s12, v58, v100
	v_bfi_b32 v101, s12, v101, v59
	v_lshrrev_b32_e32 v60, 1, v103
	v_lshlrev_b32_e32 v61, 1, v102
	v_bfi_b32 v102, s12, v60, v102
	v_bfi_b32 v103, s12, v103, v61
	v_lshrrev_b32_e32 v58, 1, v105
	v_lshlrev_b32_e32 v59, 1, v104
	v_bfi_b32 v104, s12, v58, v104
	v_bfi_b32 v105, s12, v105, v59
	v_lshrrev_b32_e32 v60, 1, v107
	v_lshlrev_b32_e32 v61, 1, v106
	v_bfi_b32 v106, s12, v60, v106
	v_bfi_b32 v107, s12, v107, v61
	s_mov_b32 s12, 0x07060302
	s_mov_b32 s19, 0x05040100
	v_perm_b32 v63, v108, v124, s12
	v_perm_b32 v124, v108, v124, s19
	v_perm_b32 v108, v109, v125, s12
	v_perm_b32 v125, v109, v125, s19
	v_perm_b32 v109, v110, v126, s12
	v_perm_b32 v126, v110, v126, s19
	v_perm_b32 v110, v111, v127, s12
	v_perm_b32 v127, v111, v127, s19
	v_perm_b32 v111, v112, v128, s12
	v_perm_b32 v128, v112, v128, s19
	v_perm_b32 v112, v113, v129, s12
	v_perm_b32 v129, v113, v129, s19
	v_perm_b32 v113, v114, v130, s12
	v_perm_b32 v130, v114, v130, s19
	v_perm_b32 v114, v115, v131, s12
	v_perm_b32 v131, v115, v131, s19
	v_perm_b32 v115, v116, v132, s12
	v_perm_b32 v132, v116, v132, s19
	v_perm_b32 v116, v117, v133, s12
	v_perm_b32 v133, v117, v133, s19
	v_perm_b32 v117, v118, v134, s12
	v_perm_b32 v134, v118, v134, s19
	v_perm_b32 v118, v119, v135, s12
	v_perm_b32 v135, v119, v135, s19
	v_perm_b32 v119, v120, v136, s12
	v_perm_b32 v136, v120, v136, s19
	v_perm_b32 v120, v121, v137, s12
	v_perm_b32 v137, v121, v137, s19
	v_perm_b32 v121, v122, v138, s12
	v_perm_b32 v138, v122, v138, s19
	v_perm_b32 v122, v123, v139, s12
	v_perm_b32 v139, v123, v139, s19
	s_mov_b32 s12, 0x07030501
	s_mov_b32 s19, 0x06020400
	v_perm_b32 v123, v63, v115, s12
	v_perm_b32 v115, v63, v115, s19
	v_perm_b32 v63, v108, v116, s12
	v_perm_b32 v116, v108, v116, s19
	v_perm_b32 v108, v109, v117, s12
	v_perm_b32 v117, v109, v117, s19
	v_perm_b32 v109, v110, v118, s12
	v_perm_b32 v118, v110, v118, s19
	v_perm_b32 v110, v111, v119, s12
	v_perm_b32 v119, v111, v119, s19
	v_perm_b32 v111, v112, v120, s12
	v_perm_b32 v120, v112, v120, s19
	v_perm_b32 v112, v113, v121, s12
	v_perm_b32 v121, v113, v121, s19
	v_perm_b32 v113, v114, v122, s12
	v_perm_b32 v122, v114, v122, s19
	v_perm_b32 v114, v124, v132, s12
	v_perm_b32 v132, v124, v132, s19
	v_perm_b32 v124, v125, v133, s12
	v_perm_b32 v133, v125, v133, s19
	v_perm_b32 v125, v126, v134, s12
	v_perm_b32 v134, v126, v134, s19
	v_perm_b32 v126, v127, v135, s12
	v_perm_b32 v135, v127, v135, s19
	v_perm_b32 v127, v128, v136, s12
	v_perm_b32 v136, v128, v136, s19
	v_perm_b32 v128, v129, v137, s12
	v_perm_b32 v137, v129, v137, s19
	v_perm_b32 v129, v130, v138, s12
	v_perm_b32 v138, v130, v138, s19
	v_perm_b32 v130, v131, v139, s12
	v_perm_b32 v139, v131, v139, s19
	s_mov_b32 s12, 0x0f0f0f0f
	v_lshrrev_b32_e32 v58, 4, v110
	v_lshlrev_b32_e32 v59, 4, v123
	v_bfi_b32 v123, s12, v58, v123
	v_bfi_b32 v110, s12, v110, v59
	v_lshrrev_b32_e32 v60, 4, v111
	v_lshlrev_b32_e32 v61, 4, v63
	v_bfi_b32 v63, s12, v60, v63
	v_bfi_b32 v111, s12, v111, v61
	v_lshrrev_b32_e32 v58, 4, v112
	v_lshlrev_b32_e32 v59, 4, v108
	v_bfi_b32 v108, s12, v58, v108
	v_bfi_b32 v112, s12, v112, v59
	v_lshrrev_b32_e32 v60, 4, v113
	v_lshlrev_b32_e32 v61, 4, v109
	v_bfi_b32 v109, s12, v60, v109
	v_bfi_b32 v113, s12, v113, v61
	v_lshrrev_b32_e32 v58, 4, v119
	v_lshlrev_b32_e32 v59, 4, v115
	v_bfi_b32 v115, s12, v58, v115
	v_bfi_b32 v119, s12, v119, v59
	v_lshrrev_b32_e32 v60, 4, v120
	v_lshlrev_b32_e32 v61, 4, v116
	v_bfi_b32 v116, s12, v60, v116
	v_bfi_b32 v120, s12, v120, v61
	v_lshrrev_b32_e32 v58, 4, v121
	v_lshlrev_b32_e32 v59, 4, v117
	v_bfi_b32 v117, s12, v58, v117
	v_bfi_b32 v121, s12, v121, v59
	v_lshrrev_b32_e32 v60, 4, v122
	v_lshlrev_b32_e32 v61, 4, v118
	v_bfi_b32 v118, s12, v60, v118
	v_bfi_b32 v122, s12, v122, v61
	v_lshrrev_b32_e32 v58, 4, v127
	v_lshlrev_b32_e32 v59, 4, v114
	v_bfi_b32 v114, s12, v58, v114
	v_bfi_b32 v127, s12, v127, v59
	v_lshrrev_b32_e32 v60, 4, v128
	v_lshlrev_b32_e32 v61, 4, v124
	v_bfi_b32 v124, s12, v60, v124
	v_bfi_b32 v128, s12, v128, v61
	v_lshrrev_b32_e32 v58, 4, v129
	v_lshlrev_b32_e32 v59, 4, v125
	v_bfi_b32 v125, s12, v58, v125
	v_bfi_b32 v129, s12, v129, v59
	v_lshrrev_b32_e32 v60, 4, v130
	v_lshlrev_b32_e32 v61, 4, v126
	v_bfi_b32 v126, s12, v60, v126
	v_bfi_b32 v130, s12, v130, v61
	v_lshrrev_b32_e32 v58, 4, v136
	v_lshlrev_b32_e32 v59, 4, v132
	v_bfi_b32 v132, s12, v58, v132
	v_bfi_b32 v136, s12, v136, v59
	v_lshrrev_b32_e32 v60, 4, v137
	v_lshlrev_b32_e32 v61, 4, v133
	v_bfi_b32 v133, s12, v60, v133
	v_bfi_b32 v137, s12, v137, v61
	v_lshrrev_b32_e32 v58, 4, v138
	v_lshlrev_b32_e32 v59, 4, v134
	v_bfi_b32 v134, s12, v58, v134
	v_bfi_b32 v138, s12, v138, v59
	v_lshrrev_b32_e32 v60, 4, v139
	v_lshlrev_b32_e32 v61, 4, v135
	v_bfi_b32 v135, s12, v60, v135
	v_bfi_b32 v139, s12, v139, v61
	s_mov_b32 s12, 0x33333333
	v_lshrrev_b32_e32 v58, 2, v108
	v_lshlrev_b32_e32 v59, 2, v123
	v_bfi_b32 v123, s12, v58, v123
	v_bfi_b32 v108, s12, v108, v59
	v_lshrrev_b32_e32 v60, 2, v109
	v_lshlrev_b32_e32 v61, 2, v63
	v_bfi_b32 v63, s12, v60, v63
	v_bfi_b32 v109, s12, v109, v61
	v_lshrrev_b32_e32 v58, 2, v112
	v_lshlrev_b32_e32 v59, 2, v110
	v_bfi_b32 v110, s12, v58, v110
	v_bfi_b32 v112, s12, v112, v59
	v_lshrrev_b32_e32 v60, 2, v113
	v_lshlrev_b32_e32 v61, 2, v111
	v_bfi_b32 v111, s12, v60, v111
	v_bfi_b32 v113, s12, v113, v61
	v_lshrrev_b32_e32 v58, 2, v117
	v_lshlrev_b32_e32 v59, 2, v115
	v_bfi_b32 v115, s12, v58, v115
	v_bfi_b32 v117, s12, v117, v59
	v_lshrrev_b32_e32 v60, 2, v118
	v_lshlrev_b32_e32 v61, 2, v116
	v_bfi_b32 v116, s12, v60, v116
	v_bfi_b32 v118, s12, v118, v61
	v_lshrrev_b32_e32 v58, 2, v121
	v_lshlrev_b32_e32 v59, 2, v119
	v_bfi_b32 v119, s12, v58, v119
	v_bfi_b32 v121, s12, v121, v59
	v_lshrrev_b32_e32 v60, 2, v122
	v_lshlrev_b32_e32 v61, 2, v120
	v_bfi_b32 v120, s12, v60, v120
	v_bfi_b32 v122, s12, v122, v61
	v_lshrrev_b32_e32 v58, 2, v125
	v_lshlrev_b32_e32 v59, 2, v114
	v_bfi_b32 v114, s12, v58, v114
	v_bfi_b32 v125, s12, v125, v59
	v_lshrrev_b32_e32 v60, 2, v126
	v_lshlrev_b32_e32 v61, 2, v124
	v_bfi_b32 v124, s12, v60, v124
	v_bfi_b32 v126, s12, v126, v61
	v_lshrrev_b32_e32 v58, 2, v129
	v_lshlrev_b32_e32 v59, 2, v127
	v_bfi_b32 v127, s12, v58, v127
	v_bfi_b32 v129, s12, v129, v59
	v_lshrrev_b32_e32 v60, 2, v130
	v_lshlrev_b32_e32 v61, 2, v128
	v_bfi_b32 v128, s12, v60, v128
	v_bfi_b32 v130, s12, v130, v61
	v_lshrrev_b32_e32 v58, 2, v134
	v_lshlrev_b32_e32 v59, 2, v132
	v_bfi_b32 v132, s12, v58, v132
	v_bfi_b32 v134, s12, v134, v59
	v_lshrrev_b32_e32 v60, 2, v135
	v_lshlrev_b32_e32 v61, 2, v133
	v_bfi_b32 v133, s12, v60, v133
	v_bfi_b32 v135, s12, v135, v61
	v_lshrrev_b32_e32 v58, 2, v138
	v_lshlrev_b32_e32 v59, 2, v136
	v_bfi_b32 v136, s12, v58, v136
	v_bfi_b32 v138, s12, v138, v59
	v_lshrrev_b32_e32 v60, 2, v139
	v_lshlrev_b32_e32 v61, 2, v137
	v_bfi_b32 v137, s12, v60, v137
	v_bfi_b32 v139, s12, v139, v61
	s_mov_b32 s12, 0x55555555
	v_lshrrev_b32_e32 v58, 1, v63
	v_lshlrev_b32_e32 v59, 1, v123
	v_bfi_b32 v123, s12, v58, v123
	v_bfi_b32 v63, s12, v63, v59
	v_lshrrev_b32_e32 v60, 1, v109
	v_lshlrev_b32_e32 v61, 1, v108
	v_bfi_b32 v108, s12, v60, v108
	v_bfi_b32 v109, s12, v109, v61
	v_lshrrev_b32_e32 v58, 1, v111
	v_lshlrev_b32_e32 v59, 1, v110
	v_bfi_b32 v110, s12, v58, v110
	v_bfi_b32 v111, s12, v111, v59
	v_lshrrev_b32_e32 v60, 1, v113
	v_lshlrev_b32_e32 v61, 1, v112
	v_bfi_b32 v112, s12, v60, v112
	v_bfi_b32 v113, s12, v113, v61
	v_lshrrev_b32_e32 v58, 1, v116
	v_lshlrev_b32_e32 v59, 1, v115
	v_bfi_b32 v115, s12, v58, v115
	v_bfi_b32 v116, s12, v116, v59
	v_lshrrev_b32_e32 v60, 1, v118
	v_lshlrev_b32_e32 v61, 1, v117
	v_bfi_b32 v117, s12, v60, v117
	v_bfi_b32 v118, s12, v118, v61
	v_lshrrev_b32_e32 v58, 1, v120
	v_lshlrev_b32_e32 v59, 1, v119
	v_bfi_b32 v119, s12, v58, v119
	v_bfi_b32 v120, s12, v120, v59
	v_lshrrev_b32_e32 v60, 1, v122
	v_lshlrev_b32_e32 v61, 1, v121
	v_bfi_b32 v121, s12, v60, v121
	v_bfi_b32 v122, s12, v122, v61
	v_lshrrev_b32_e32 v58, 1, v124
	v_lshlrev_b32_e32 v59, 1, v114
	v_bfi_b32 v114, s12, v58, v114
	v_bfi_b32 v124, s12, v124, v59
	v_lshrrev_b32_e32 v60, 1, v126
	v_lshlrev_b32_e32 v61, 1, v125
	v_bfi_b32 v125, s12, v60, v125
	v_bfi_b32 v126, s12, v126, v61
	v_lshrrev_b32_e32 v58, 1, v128
	v_lshlrev_b32_e32 v59, 1, v127
	v_bfi_b32 v127, s12, v58, v127
	v_bfi_b32 v128, s12, v128, v59
	v_lshrrev_b32_e32 v60, 1, v130
	v_lshlrev_b32_e32 v61, 1, v129
	v_bfi_b32 v129, s12, v60, v129
	v_bfi_b32 v130, s12, v130, v61
	v_lshrrev_b32_e32 v58, 1, v133
	v_lshlrev_b32_e32 v59, 1, v132
	v_bfi_b32 v132, s12, v58, v132
	v_bfi_b32 v133, s12, v133, v59
	v_lshrrev_b32_e32 v60, 1, v135
	v_lshlrev_b32_e32 v61, 1, v134
	v_bfi_b32 v134, s12, v60, v134
	v_bfi_b32 v135, s12, v135, v61
	v_lshrrev_b32_e32 v58, 1, v137
	v_lshlrev_b32_e32 v59, 1, v136
	v_bfi_b32 v136, s12, v58, v136
	v_bfi_b32 v137, s12, v137, v59
	v_lshrrev_b32_e32 v60, 1, v139
	v_lshlrev_b32_e32 v61, 1, v138
	v_bfi_b32 v138, s12, v60, v138
	v_bfi_b32 v139, s12, v139, v61
.Lmy_s2_p0:
	v_and_b32_e32 v50, v10, v91
	v_and_b32_e32 v51, v11, v123
	v_bcnt_u32_b32 v52, v50, v14
	v_bcnt_u32_b32 v52, v51, v52
	s_nop 1
	v_add_u32_dpp v53, v52, v52 quad_perm:[1,0,3,2] row_mask:0xf bank_mask:0xf bound_ctrl:1
	s_nop 1
	v_add_u32_dpp v53, v53, v53 quad_perm:[2,3,0,1] row_mask:0xf bank_mask:0xf bound_ctrl:1
	s_nop 1
	v_add_u32_dpp v53, v53, v53 row_half_mirror row_mask:0xf bank_mask:0xf bound_ctrl:1
	s_nop 1
	v_add_u32_dpp v53, v53, v53 row_mirror row_mask:0xf bank_mask:0xf bound_ctrl:1
	v_mov_b32_e32 v54, v53
	s_nop 1
	v_permlane16_swap_b32 v53, v54
	v_add_u32_e32 v53, v53, v54
	v_cmp_gt_i32_e32 vcc, 0x100, v53
	v_cmp_eq_u32_e64 s[8:9], v53, v15
	s_nop 0
	v_cndmask_b32_e64 v55, 0, -1, vcc
	v_cndmask_b32_e32 v14, v14, v52, vcc
	v_bitop3_b32 v12, v12, v50, v55 bitop3:0xf8
	v_bitop3_b32 v13, v13, v51, v55 bitop3:0xf8
	v_bitop3_b32 v10, v10, v91, v55 bitop3:0x60
	v_bitop3_b32 v11, v11, v123, v55 bitop3:0x60
	s_cmp_lg_u64 s[8:9], 0
	s_cbranch_scc1 .Lmy_s2_h0
.Lmy_s2_p1:
	v_and_b32_e32 v50, v10, v62
	v_and_b32_e32 v51, v11, v63
	v_bcnt_u32_b32 v52, v50, v14
	v_bcnt_u32_b32 v52, v51, v52
	s_nop 1
	v_add_u32_dpp v53, v52, v52 quad_perm:[1,0,3,2] row_mask:0xf bank_mask:0xf bound_ctrl:1
	s_nop 1
	v_add_u32_dpp v53, v53, v53 quad_perm:[2,3,0,1] row_mask:0xf bank_mask:0xf bound_ctrl:1
	s_nop 1
	v_add_u32_dpp v53, v53, v53 row_half_mirror row_mask:0xf bank_mask:0xf bound_ctrl:1
	s_nop 1
	v_add_u32_dpp v53, v53, v53 row_mirror row_mask:0xf bank_mask:0xf bound_ctrl:1
	v_mov_b32_e32 v54, v53
	s_nop 1
	v_permlane16_swap_b32 v53, v54
	v_add_u32_e32 v53, v53, v54
	v_cmp_gt_i32_e32 vcc, 0x100, v53
	v_cmp_eq_u32_e64 s[8:9], v53, v15
	s_nop 0
	v_cndmask_b32_e64 v55, 0, -1, vcc
	v_cndmask_b32_e32 v14, v14, v52, vcc
	v_bitop3_b32 v12, v12, v50, v55 bitop3:0xf8
	v_bitop3_b32 v13, v13, v51, v55 bitop3:0xf8
	v_bitop3_b32 v10, v10, v62, v55 bitop3:0x60
	v_bitop3_b32 v11, v11, v63, v55 bitop3:0x60
	s_cmp_lg_u64 s[8:9], 0
	s_cbranch_scc1 .Lmy_s2_h1
.Lmy_s2_p2:
	v_and_b32_e32 v50, v10, v76
	v_and_b32_e32 v51, v11, v108
	v_bcnt_u32_b32 v52, v50, v14
	v_bcnt_u32_b32 v52, v51, v52
	s_nop 1
	v_add_u32_dpp v53, v52, v52 quad_perm:[1,0,3,2] row_mask:0xf bank_mask:0xf bound_ctrl:1
	s_nop 1
	v_add_u32_dpp v53, v53, v53 quad_perm:[2,3,0,1] row_mask:0xf bank_mask:0xf bound_ctrl:1
	s_nop 1
	v_add_u32_dpp v53, v53, v53 row_half_mirror row_mask:0xf bank_mask:0xf bound_ctrl:1
	s_nop 1
	v_add_u32_dpp v53, v53, v53 row_mirror row_mask:0xf bank_mask:0xf bound_ctrl:1
	v_mov_b32_e32 v54, v53
	s_nop 1
	v_permlane16_swap_b32 v53, v54
	v_add_u32_e32 v53, v53, v54
	v_cmp_gt_i32_e32 vcc, 0x100, v53
	v_cmp_eq_u32_e64 s[8:9], v53, v15
	s_nop 0
	v_cndmask_b32_e64 v55, 0, -1, vcc
	v_cndmask_b32_e32 v14, v14, v52, vcc
	v_bitop3_b32 v12, v12, v50, v55 bitop3:0xf8
	v_bitop3_b32 v13, v13, v51, v55 bitop3:0xf8
	v_bitop3_b32 v10, v10, v76, v55 bitop3:0x60
	v_bitop3_b32 v11, v11, v108, v55 bitop3:0x60
	s_cmp_lg_u64 s[8:9], 0
	s_cbranch_scc1 .Lmy_s2_h2
.Lmy_s2_p3:
	v_and_b32_e32 v50, v10, v77
	v_and_b32_e32 v51, v11, v109
	v_bcnt_u32_b32 v52, v50, v14
	v_bcnt_u32_b32 v52, v51, v52
	s_nop 1
	v_add_u32_dpp v53, v52, v52 quad_perm:[1,0,3,2] row_mask:0xf bank_mask:0xf bound_ctrl:1
	s_nop 1
	v_add_u32_dpp v53, v53, v53 quad_perm:[2,3,0,1] row_mask:0xf bank_mask:0xf bound_ctrl:1
	s_nop 1
	v_add_u32_dpp v53, v53, v53 row_half_mirror row_mask:0xf bank_mask:0xf bound_ctrl:1
	s_nop 1
	v_add_u32_dpp v53, v53, v53 row_mirror row_mask:0xf bank_mask:0xf bound_ctrl:1
	v_mov_b32_e32 v54, v53
	s_nop 1
	v_permlane16_swap_b32 v53, v54
	v_add_u32_e32 v53, v53, v54
	v_cmp_gt_i32_e32 vcc, 0x100, v53
	v_cmp_eq_u32_e64 s[8:9], v53, v15
	s_nop 0
	v_cndmask_b32_e64 v55, 0, -1, vcc
	v_cndmask_b32_e32 v14, v14, v52, vcc
	v_bitop3_b32 v12, v12, v50, v55 bitop3:0xf8
	v_bitop3_b32 v13, v13, v51, v55 bitop3:0xf8
	v_bitop3_b32 v10, v10, v77, v55 bitop3:0x60
	v_bitop3_b32 v11, v11, v109, v55 bitop3:0x60
	s_cmp_lg_u64 s[8:9], 0
	s_cbranch_scc1 .Lmy_s2_h3
.Lmy_s2_p4:
	v_and_b32_e32 v50, v10, v78
	v_and_b32_e32 v51, v11, v110
	v_bcnt_u32_b32 v52, v50, v14
	v_bcnt_u32_b32 v52, v51, v52
	s_nop 1
	v_add_u32_dpp v53, v52, v52 quad_perm:[1,0,3,2] row_mask:0xf bank_mask:0xf bound_ctrl:1
	s_nop 1
	v_add_u32_dpp v53, v53, v53 quad_perm:[2,3,0,1] row_mask:0xf bank_mask:0xf bound_ctrl:1
	s_nop 1
	v_add_u32_dpp v53, v53, v53 row_half_mirror row_mask:0xf bank_mask:0xf bound_ctrl:1
	s_nop 1
	v_add_u32_dpp v53, v53, v53 row_mirror row_mask:0xf bank_mask:0xf bound_ctrl:1
	v_mov_b32_e32 v54, v53
	s_nop 1
	v_permlane16_swap_b32 v53, v54
	v_add_u32_e32 v53, v53, v54
	v_cmp_gt_i32_e32 vcc, 0x100, v53
	v_cmp_eq_u32_e64 s[8:9], v53, v15
	s_nop 0
	v_cndmask_b32_e64 v55, 0, -1, vcc
	v_cndmask_b32_e32 v14, v14, v52, vcc
	v_bitop3_b32 v12, v12, v50, v55 bitop3:0xf8
	v_bitop3_b32 v13, v13, v51, v55 bitop3:0xf8
	v_bitop3_b32 v10, v10, v78, v55 bitop3:0x60
	v_bitop3_b32 v11, v11, v110, v55 bitop3:0x60
	s_cmp_lg_u64 s[8:9], 0
	s_cbranch_scc1 .Lmy_s2_h4
.Lmy_s2_p5:
	v_and_b32_e32 v50, v10, v79
	v_and_b32_e32 v51, v11, v111
	v_bcnt_u32_b32 v52, v50, v14
	v_bcnt_u32_b32 v52, v51, v52
	s_nop 1
	v_add_u32_dpp v53, v52, v52 quad_perm:[1,0,3,2] row_mask:0xf bank_mask:0xf bound_ctrl:1
	s_nop 1
	v_add_u32_dpp v53, v53, v53 quad_perm:[2,3,0,1] row_mask:0xf bank_mask:0xf bound_ctrl:1
	s_nop 1
	v_add_u32_dpp v53, v53, v53 row_half_mirror row_mask:0xf bank_mask:0xf bound_ctrl:1
	s_nop 1
	v_add_u32_dpp v53, v53, v53 row_mirror row_mask:0xf bank_mask:0xf bound_ctrl:1
	v_mov_b32_e32 v54, v53
	s_nop 1
	v_permlane16_swap_b32 v53, v54
	v_add_u32_e32 v53, v53, v54
	v_cmp_gt_i32_e32 vcc, 0x100, v53
	v_cmp_eq_u32_e64 s[8:9], v53, v15
	s_nop 0
	v_cndmask_b32_e64 v55, 0, -1, vcc
	v_cndmask_b32_e32 v14, v14, v52, vcc
	v_bitop3_b32 v12, v12, v50, v55 bitop3:0xf8
	v_bitop3_b32 v13, v13, v51, v55 bitop3:0xf8
	v_bitop3_b32 v10, v10, v79, v55 bitop3:0x60
	v_bitop3_b32 v11, v11, v111, v55 bitop3:0x60
	s_cmp_lg_u64 s[8:9], 0
	s_cbranch_scc1 .Lmy_s2_h5
.Lmy_s2_p6:
	v_and_b32_e32 v50, v10, v80
	v_and_b32_e32 v51, v11, v112
	v_bcnt_u32_b32 v52, v50, v14
	v_bcnt_u32_b32 v52, v51, v52
	s_nop 1
	v_add_u32_dpp v53, v52, v52 quad_perm:[1,0,3,2] row_mask:0xf bank_mask:0xf bound_ctrl:1
	s_nop 1
	v_add_u32_dpp v53, v53, v53 quad_perm:[2,3,0,1] row_mask:0xf bank_mask:0xf bound_ctrl:1
	s_nop 1
	v_add_u32_dpp v53, v53, v53 row_half_mirror row_mask:0xf bank_mask:0xf bound_ctrl:1
	s_nop 1
	v_add_u32_dpp v53, v53, v53 row_mirror row_mask:0xf bank_mask:0xf bound_ctrl:1
	v_mov_b32_e32 v54, v53
	s_nop 1
	v_permlane16_swap_b32 v53, v54
	v_add_u32_e32 v53, v53, v54
	v_cmp_gt_i32_e32 vcc, 0x100, v53
	v_cmp_eq_u32_e64 s[8:9], v53, v15
	s_nop 0
	v_cndmask_b32_e64 v55, 0, -1, vcc
	v_cndmask_b32_e32 v14, v14, v52, vcc
	v_bitop3_b32 v12, v12, v50, v55 bitop3:0xf8
	v_bitop3_b32 v13, v13, v51, v55 bitop3:0xf8
	v_bitop3_b32 v10, v10, v80, v55 bitop3:0x60
	v_bitop3_b32 v11, v11, v112, v55 bitop3:0x60
	s_cmp_lg_u64 s[8:9], 0
	s_cbranch_scc1 .Lmy_s2_h6
.Lmy_s2_p7:
	v_and_b32_e32 v50, v10, v81
	v_and_b32_e32 v51, v11, v113
	v_bcnt_u32_b32 v52, v50, v14
	v_bcnt_u32_b32 v52, v51, v52
	s_nop 1
	v_add_u32_dpp v53, v52, v52 quad_perm:[1,0,3,2] row_mask:0xf bank_mask:0xf bound_ctrl:1
	s_nop 1
	v_add_u32_dpp v53, v53, v53 quad_perm:[2,3,0,1] row_mask:0xf bank_mask:0xf bound_ctrl:1
	s_nop 1
	v_add_u32_dpp v53, v53, v53 row_half_mirror row_mask:0xf bank_mask:0xf bound_ctrl:1
	s_nop 1
	v_add_u32_dpp v53, v53, v53 row_mirror row_mask:0xf bank_mask:0xf bound_ctrl:1
	v_mov_b32_e32 v54, v53
	s_nop 1
	v_permlane16_swap_b32 v53, v54
	v_add_u32_e32 v53, v53, v54
	v_cmp_gt_i32_e32 vcc, 0x100, v53
	v_cmp_eq_u32_e64 s[8:9], v53, v15
	s_nop 0
	v_cndmask_b32_e64 v55, 0, -1, vcc
	v_cndmask_b32_e32 v14, v14, v52, vcc
	v_bitop3_b32 v12, v12, v50, v55 bitop3:0xf8
	v_bitop3_b32 v13, v13, v51, v55 bitop3:0xf8
	v_bitop3_b32 v10, v10, v81, v55 bitop3:0x60
	v_bitop3_b32 v11, v11, v113, v55 bitop3:0x60
	s_cmp_lg_u64 s[8:9], 0
	s_cbranch_scc1 .Lmy_s2_h7
.Lmy_s2_p8:
	v_and_b32_e32 v50, v10, v83
	v_and_b32_e32 v51, v11, v115
	v_bcnt_u32_b32 v52, v50, v14
	v_bcnt_u32_b32 v52, v51, v52
	s_nop 1
	v_add_u32_dpp v53, v52, v52 quad_perm:[1,0,3,2] row_mask:0xf bank_mask:0xf bound_ctrl:1
	s_nop 1
	v_add_u32_dpp v53, v53, v53 quad_perm:[2,3,0,1] row_mask:0xf bank_mask:0xf bound_ctrl:1
	s_nop 1
	v_add_u32_dpp v53, v53, v53 row_half_mirror row_mask:0xf bank_mask:0xf bound_ctrl:1
	s_nop 1
	v_add_u32_dpp v53, v53, v53 row_mirror row_mask:0xf bank_mask:0xf bound_ctrl:1
	v_mov_b32_e32 v54, v53
	s_nop 1
	v_permlane16_swap_b32 v53, v54
	v_add_u32_e32 v53, v53, v54
	v_cmp_gt_i32_e32 vcc, 0x100, v53
	v_cmp_eq_u32_e64 s[8:9], v53, v15
	s_nop 0
	v_cndmask_b32_e64 v55, 0, -1, vcc
	v_cndmask_b32_e32 v14, v14, v52, vcc
	v_bitop3_b32 v12, v12, v50, v55 bitop3:0xf8
	v_bitop3_b32 v13, v13, v51, v55 bitop3:0xf8
	v_bitop3_b32 v10, v10, v83, v55 bitop3:0x60
	v_bitop3_b32 v11, v11, v115, v55 bitop3:0x60
	s_cmp_lg_u64 s[8:9], 0
	s_cbranch_scc1 .Lmy_s2_h8
.Lmy_s2_p9:
	v_and_b32_e32 v50, v10, v84
	v_and_b32_e32 v51, v11, v116
	v_bcnt_u32_b32 v52, v50, v14
	v_bcnt_u32_b32 v52, v51, v52
	s_nop 1
	v_add_u32_dpp v53, v52, v52 quad_perm:[1,0,3,2] row_mask:0xf bank_mask:0xf bound_ctrl:1
	s_nop 1
	v_add_u32_dpp v53, v53, v53 quad_perm:[2,3,0,1] row_mask:0xf bank_mask:0xf bound_ctrl:1
	s_nop 1
	v_add_u32_dpp v53, v53, v53 row_half_mirror row_mask:0xf bank_mask:0xf bound_ctrl:1
	s_nop 1
	v_add_u32_dpp v53, v53, v53 row_mirror row_mask:0xf bank_mask:0xf bound_ctrl:1
	v_mov_b32_e32 v54, v53
	s_nop 1
	v_permlane16_swap_b32 v53, v54
	v_add_u32_e32 v53, v53, v54
	v_cmp_gt_i32_e32 vcc, 0x100, v53
	v_cmp_eq_u32_e64 s[8:9], v53, v15
	s_nop 0
	v_cndmask_b32_e64 v55, 0, -1, vcc
	v_cndmask_b32_e32 v14, v14, v52, vcc
	v_bitop3_b32 v12, v12, v50, v55 bitop3:0xf8
	v_bitop3_b32 v13, v13, v51, v55 bitop3:0xf8
	v_bitop3_b32 v10, v10, v84, v55 bitop3:0x60
	v_bitop3_b32 v11, v11, v116, v55 bitop3:0x60
	s_cmp_lg_u64 s[8:9], 0
	s_cbranch_scc1 .Lmy_s2_h9
.Lmy_s2_p10:
	v_and_b32_e32 v50, v10, v85
	v_and_b32_e32 v51, v11, v117
	v_bcnt_u32_b32 v52, v50, v14
	v_bcnt_u32_b32 v52, v51, v52
	s_nop 1
	v_add_u32_dpp v53, v52, v52 quad_perm:[1,0,3,2] row_mask:0xf bank_mask:0xf bound_ctrl:1
	s_nop 1
	v_add_u32_dpp v53, v53, v53 quad_perm:[2,3,0,1] row_mask:0xf bank_mask:0xf bound_ctrl:1
	s_nop 1
	v_add_u32_dpp v53, v53, v53 row_half_mirror row_mask:0xf bank_mask:0xf bound_ctrl:1
	s_nop 1
	v_add_u32_dpp v53, v53, v53 row_mirror row_mask:0xf bank_mask:0xf bound_ctrl:1
	v_mov_b32_e32 v54, v53
	s_nop 1
	v_permlane16_swap_b32 v53, v54
	v_add_u32_e32 v53, v53, v54
	v_cmp_gt_i32_e32 vcc, 0x100, v53
	v_cmp_eq_u32_e64 s[8:9], v53, v15
	s_nop 0
	v_cndmask_b32_e64 v55, 0, -1, vcc
	v_cndmask_b32_e32 v14, v14, v52, vcc
	v_bitop3_b32 v12, v12, v50, v55 bitop3:0xf8
	v_bitop3_b32 v13, v13, v51, v55 bitop3:0xf8
	v_bitop3_b32 v10, v10, v85, v55 bitop3:0x60
	v_bitop3_b32 v11, v11, v117, v55 bitop3:0x60
	s_cmp_lg_u64 s[8:9], 0
	s_cbranch_scc1 .Lmy_s2_h10
.Lmy_s2_p11:
	v_and_b32_e32 v50, v10, v86
	v_and_b32_e32 v51, v11, v118
	v_bcnt_u32_b32 v52, v50, v14
	v_bcnt_u32_b32 v52, v51, v52
	s_nop 1
	v_add_u32_dpp v53, v52, v52 quad_perm:[1,0,3,2] row_mask:0xf bank_mask:0xf bound_ctrl:1
	s_nop 1
	v_add_u32_dpp v53, v53, v53 quad_perm:[2,3,0,1] row_mask:0xf bank_mask:0xf bound_ctrl:1
	s_nop 1
	v_add_u32_dpp v53, v53, v53 row_half_mirror row_mask:0xf bank_mask:0xf bound_ctrl:1
	s_nop 1
	v_add_u32_dpp v53, v53, v53 row_mirror row_mask:0xf bank_mask:0xf bound_ctrl:1
	v_mov_b32_e32 v54, v53
	s_nop 1
	v_permlane16_swap_b32 v53, v54
	v_add_u32_e32 v53, v53, v54
	v_cmp_gt_i32_e32 vcc, 0x100, v53
	v_cmp_eq_u32_e64 s[8:9], v53, v15
	s_nop 0
	v_cndmask_b32_e64 v55, 0, -1, vcc
	v_cndmask_b32_e32 v14, v14, v52, vcc
	v_bitop3_b32 v12, v12, v50, v55 bitop3:0xf8
	v_bitop3_b32 v13, v13, v51, v55 bitop3:0xf8
	v_bitop3_b32 v10, v10, v86, v55 bitop3:0x60
	v_bitop3_b32 v11, v11, v118, v55 bitop3:0x60
	s_cmp_lg_u64 s[8:9], 0
	s_cbranch_scc1 .Lmy_s2_h11
.Lmy_s2_p12:
	v_and_b32_e32 v50, v10, v87
	v_and_b32_e32 v51, v11, v119
	v_bcnt_u32_b32 v52, v50, v14
	v_bcnt_u32_b32 v52, v51, v52
	s_nop 1
	v_add_u32_dpp v53, v52, v52 quad_perm:[1,0,3,2] row_mask:0xf bank_mask:0xf bound_ctrl:1
	s_nop 1
	v_add_u32_dpp v53, v53, v53 quad_perm:[2,3,0,1] row_mask:0xf bank_mask:0xf bound_ctrl:1
	s_nop 1
	v_add_u32_dpp v53, v53, v53 row_half_mirror row_mask:0xf bank_mask:0xf bound_ctrl:1
	s_nop 1
	v_add_u32_dpp v53, v53, v53 row_mirror row_mask:0xf bank_mask:0xf bound_ctrl:1
	v_mov_b32_e32 v54, v53
	s_nop 1
	v_permlane16_swap_b32 v53, v54
	v_add_u32_e32 v53, v53, v54
	v_cmp_gt_i32_e32 vcc, 0x100, v53
	v_cmp_eq_u32_e64 s[8:9], v53, v15
	s_nop 0
	v_cndmask_b32_e64 v55, 0, -1, vcc
	v_cndmask_b32_e32 v14, v14, v52, vcc
	v_bitop3_b32 v12, v12, v50, v55 bitop3:0xf8
	v_bitop3_b32 v13, v13, v51, v55 bitop3:0xf8
	v_bitop3_b32 v10, v10, v87, v55 bitop3:0x60
	v_bitop3_b32 v11, v11, v119, v55 bitop3:0x60
	s_cmp_lg_u64 s[8:9], 0
	s_cbranch_scc1 .Lmy_s2_h12
.Lmy_s2_p13:
	v_and_b32_e32 v50, v10, v88
	v_and_b32_e32 v51, v11, v120
	v_bcnt_u32_b32 v52, v50, v14
	v_bcnt_u32_b32 v52, v51, v52
	s_nop 1
	v_add_u32_dpp v53, v52, v52 quad_perm:[1,0,3,2] row_mask:0xf bank_mask:0xf bound_ctrl:1
	s_nop 1
	v_add_u32_dpp v53, v53, v53 quad_perm:[2,3,0,1] row_mask:0xf bank_mask:0xf bound_ctrl:1
	s_nop 1
	v_add_u32_dpp v53, v53, v53 row_half_mirror row_mask:0xf bank_mask:0xf bound_ctrl:1
	s_nop 1
	v_add_u32_dpp v53, v53, v53 row_mirror row_mask:0xf bank_mask:0xf bound_ctrl:1
	v_mov_b32_e32 v54, v53
	s_nop 1
	v_permlane16_swap_b32 v53, v54
	v_add_u32_e32 v53, v53, v54
	v_cmp_gt_i32_e32 vcc, 0x100, v53
	v_cmp_eq_u32_e64 s[8:9], v53, v15
	s_nop 0
	v_cndmask_b32_e64 v55, 0, -1, vcc
	v_cndmask_b32_e32 v14, v14, v52, vcc
	v_bitop3_b32 v12, v12, v50, v55 bitop3:0xf8
	v_bitop3_b32 v13, v13, v51, v55 bitop3:0xf8
	v_bitop3_b32 v10, v10, v88, v55 bitop3:0x60
	v_bitop3_b32 v11, v11, v120, v55 bitop3:0x60
	s_cmp_lg_u64 s[8:9], 0
	s_cbranch_scc1 .Lmy_s2_h13
.Lmy_s2_p14:
	v_and_b32_e32 v50, v10, v89
	v_and_b32_e32 v51, v11, v121
	v_bcnt_u32_b32 v52, v50, v14
	v_bcnt_u32_b32 v52, v51, v52
	s_nop 1
	v_add_u32_dpp v53, v52, v52 quad_perm:[1,0,3,2] row_mask:0xf bank_mask:0xf bound_ctrl:1
	s_nop 1
	v_add_u32_dpp v53, v53, v53 quad_perm:[2,3,0,1] row_mask:0xf bank_mask:0xf bound_ctrl:1
	s_nop 1
	v_add_u32_dpp v53, v53, v53 row_half_mirror row_mask:0xf bank_mask:0xf bound_ctrl:1
	s_nop 1
	v_add_u32_dpp v53, v53, v53 row_mirror row_mask:0xf bank_mask:0xf bound_ctrl:1
	v_mov_b32_e32 v54, v53
	s_nop 1
	v_permlane16_swap_b32 v53, v54
	v_add_u32_e32 v53, v53, v54
	v_cmp_gt_i32_e32 vcc, 0x100, v53
	v_cmp_eq_u32_e64 s[8:9], v53, v15
	s_nop 0
	v_cndmask_b32_e64 v55, 0, -1, vcc
	v_cndmask_b32_e32 v14, v14, v52, vcc
	v_bitop3_b32 v12, v12, v50, v55 bitop3:0xf8
	v_bitop3_b32 v13, v13, v51, v55 bitop3:0xf8
	v_bitop3_b32 v10, v10, v89, v55 bitop3:0x60
	v_bitop3_b32 v11, v11, v121, v55 bitop3:0x60
	s_cmp_lg_u64 s[8:9], 0
	s_cbranch_scc1 .Lmy_s2_h14
.Lmy_s2_p15:
	v_and_b32_e32 v50, v10, v90
	v_and_b32_e32 v51, v11, v122
	v_bcnt_u32_b32 v52, v50, v14
	v_bcnt_u32_b32 v52, v51, v52
	s_nop 1
	v_add_u32_dpp v53, v52, v52 quad_perm:[1,0,3,2] row_mask:0xf bank_mask:0xf bound_ctrl:1
	s_nop 1
	v_add_u32_dpp v53, v53, v53 quad_perm:[2,3,0,1] row_mask:0xf bank_mask:0xf bound_ctrl:1
	s_nop 1
	v_add_u32_dpp v53, v53, v53 row_half_mirror row_mask:0xf bank_mask:0xf bound_ctrl:1
	s_nop 1
	v_add_u32_dpp v53, v53, v53 row_mirror row_mask:0xf bank_mask:0xf bound_ctrl:1
	v_mov_b32_e32 v54, v53
	s_nop 1
	v_permlane16_swap_b32 v53, v54
	v_add_u32_e32 v53, v53, v54
	v_cmp_gt_i32_e32 vcc, 0x100, v53
	v_cmp_eq_u32_e64 s[8:9], v53, v15
	s_nop 0
	v_cndmask_b32_e64 v55, 0, -1, vcc
	v_cndmask_b32_e32 v14, v14, v52, vcc
	v_bitop3_b32 v12, v12, v50, v55 bitop3:0xf8
	v_bitop3_b32 v13, v13, v51, v55 bitop3:0xf8
	v_bitop3_b32 v10, v10, v90, v55 bitop3:0x60
	v_bitop3_b32 v11, v11, v122, v55 bitop3:0x60
	s_cmp_lg_u64 s[8:9], 0
	s_cbranch_scc1 .Lmy_s2_h15
.Lmy_s2_p16:
	v_and_b32_e32 v50, v10, v82
	v_and_b32_e32 v51, v11, v114
	v_bcnt_u32_b32 v52, v50, v14
	v_bcnt_u32_b32 v52, v51, v52
	s_nop 1
	v_add_u32_dpp v53, v52, v52 quad_perm:[1,0,3,2] row_mask:0xf bank_mask:0xf bound_ctrl:1
	s_nop 1
	v_add_u32_dpp v53, v53, v53 quad_perm:[2,3,0,1] row_mask:0xf bank_mask:0xf bound_ctrl:1
	s_nop 1
	v_add_u32_dpp v53, v53, v53 row_half_mirror row_mask:0xf bank_mask:0xf bound_ctrl:1
	s_nop 1
	v_add_u32_dpp v53, v53, v53 row_mirror row_mask:0xf bank_mask:0xf bound_ctrl:1
	v_mov_b32_e32 v54, v53
	s_nop 1
	v_permlane16_swap_b32 v53, v54
	v_add_u32_e32 v53, v53, v54
	v_cmp_gt_i32_e32 vcc, 0x100, v53
	v_cmp_eq_u32_e64 s[8:9], v53, v15
	s_nop 0
	v_cndmask_b32_e64 v55, 0, -1, vcc
	v_cndmask_b32_e32 v14, v14, v52, vcc
	v_bitop3_b32 v12, v12, v50, v55 bitop3:0xf8
	v_bitop3_b32 v13, v13, v51, v55 bitop3:0xf8
	v_bitop3_b32 v10, v10, v82, v55 bitop3:0x60
	v_bitop3_b32 v11, v11, v114, v55 bitop3:0x60
	s_cmp_lg_u64 s[8:9], 0
	s_cbranch_scc1 .Lmy_s2_h16
.Lmy_s2_p17:
	v_and_b32_e32 v50, v10, v92
	v_and_b32_e32 v51, v11, v124
	v_bcnt_u32_b32 v52, v50, v14
	v_bcnt_u32_b32 v52, v51, v52
	s_nop 1
	v_add_u32_dpp v53, v52, v52 quad_perm:[1,0,3,2] row_mask:0xf bank_mask:0xf bound_ctrl:1
	s_nop 1
	v_add_u32_dpp v53, v53, v53 quad_perm:[2,3,0,1] row_mask:0xf bank_mask:0xf bound_ctrl:1
	s_nop 1
	v_add_u32_dpp v53, v53, v53 row_half_mirror row_mask:0xf bank_mask:0xf bound_ctrl:1
	s_nop 1
	v_add_u32_dpp v53, v53, v53 row_mirror row_mask:0xf bank_mask:0xf bound_ctrl:1
	v_mov_b32_e32 v54, v53
	s_nop 1
	v_permlane16_swap_b32 v53, v54
	v_add_u32_e32 v53, v53, v54
	v_cmp_gt_i32_e32 vcc, 0x100, v53
	v_cmp_eq_u32_e64 s[8:9], v53, v15
	s_nop 0
	v_cndmask_b32_e64 v55, 0, -1, vcc
	v_cndmask_b32_e32 v14, v14, v52, vcc
	v_bitop3_b32 v12, v12, v50, v55 bitop3:0xf8
	v_bitop3_b32 v13, v13, v51, v55 bitop3:0xf8
	v_bitop3_b32 v10, v10, v92, v55 bitop3:0x60
	v_bitop3_b32 v11, v11, v124, v55 bitop3:0x60
	s_cmp_lg_u64 s[8:9], 0
	s_cbranch_scc1 .Lmy_s2_h17
.Lmy_s2_p18:
	v_and_b32_e32 v50, v10, v93
	v_and_b32_e32 v51, v11, v125
	v_bcnt_u32_b32 v52, v50, v14
	v_bcnt_u32_b32 v52, v51, v52
	s_nop 1
	v_add_u32_dpp v53, v52, v52 quad_perm:[1,0,3,2] row_mask:0xf bank_mask:0xf bound_ctrl:1
	s_nop 1
	v_add_u32_dpp v53, v53, v53 quad_perm:[2,3,0,1] row_mask:0xf bank_mask:0xf bound_ctrl:1
	s_nop 1
	v_add_u32_dpp v53, v53, v53 row_half_mirror row_mask:0xf bank_mask:0xf bound_ctrl:1
	s_nop 1
	v_add_u32_dpp v53, v53, v53 row_mirror row_mask:0xf bank_mask:0xf bound_ctrl:1
	v_mov_b32_e32 v54, v53
	s_nop 1
	v_permlane16_swap_b32 v53, v54
	v_add_u32_e32 v53, v53, v54
	v_cmp_gt_i32_e32 vcc, 0x100, v53
	v_cmp_eq_u32_e64 s[8:9], v53, v15
	s_nop 0
	v_cndmask_b32_e64 v55, 0, -1, vcc
	v_cndmask_b32_e32 v14, v14, v52, vcc
	v_bitop3_b32 v12, v12, v50, v55 bitop3:0xf8
	v_bitop3_b32 v13, v13, v51, v55 bitop3:0xf8
	v_bitop3_b32 v10, v10, v93, v55 bitop3:0x60
	v_bitop3_b32 v11, v11, v125, v55 bitop3:0x60
	s_cmp_lg_u64 s[8:9], 0
	s_cbranch_scc1 .Lmy_s2_h18
.Lmy_s2_p19:
	v_and_b32_e32 v50, v10, v94
	v_and_b32_e32 v51, v11, v126
	v_bcnt_u32_b32 v52, v50, v14
	v_bcnt_u32_b32 v52, v51, v52
	s_nop 1
	v_add_u32_dpp v53, v52, v52 quad_perm:[1,0,3,2] row_mask:0xf bank_mask:0xf bound_ctrl:1
	s_nop 1
	v_add_u32_dpp v53, v53, v53 quad_perm:[2,3,0,1] row_mask:0xf bank_mask:0xf bound_ctrl:1
	s_nop 1
	v_add_u32_dpp v53, v53, v53 row_half_mirror row_mask:0xf bank_mask:0xf bound_ctrl:1
	s_nop 1
	v_add_u32_dpp v53, v53, v53 row_mirror row_mask:0xf bank_mask:0xf bound_ctrl:1
	v_mov_b32_e32 v54, v53
	s_nop 1
	v_permlane16_swap_b32 v53, v54
	v_add_u32_e32 v53, v53, v54
	v_cmp_gt_i32_e32 vcc, 0x100, v53
	v_cmp_eq_u32_e64 s[8:9], v53, v15
	s_nop 0
	v_cndmask_b32_e64 v55, 0, -1, vcc
	v_cndmask_b32_e32 v14, v14, v52, vcc
	v_bitop3_b32 v12, v12, v50, v55 bitop3:0xf8
	v_bitop3_b32 v13, v13, v51, v55 bitop3:0xf8
	v_bitop3_b32 v10, v10, v94, v55 bitop3:0x60
	v_bitop3_b32 v11, v11, v126, v55 bitop3:0x60
	s_cmp_lg_u64 s[8:9], 0
	s_cbranch_scc1 .Lmy_s2_h19
.Lmy_s2_p20:
	v_and_b32_e32 v50, v10, v95
	v_and_b32_e32 v51, v11, v127
	v_bcnt_u32_b32 v52, v50, v14
	v_bcnt_u32_b32 v52, v51, v52
	s_nop 1
	v_add_u32_dpp v53, v52, v52 quad_perm:[1,0,3,2] row_mask:0xf bank_mask:0xf bound_ctrl:1
	s_nop 1
	v_add_u32_dpp v53, v53, v53 quad_perm:[2,3,0,1] row_mask:0xf bank_mask:0xf bound_ctrl:1
	s_nop 1
	v_add_u32_dpp v53, v53, v53 row_half_mirror row_mask:0xf bank_mask:0xf bound_ctrl:1
	s_nop 1
	v_add_u32_dpp v53, v53, v53 row_mirror row_mask:0xf bank_mask:0xf bound_ctrl:1
	v_mov_b32_e32 v54, v53
	s_nop 1
	v_permlane16_swap_b32 v53, v54
	v_add_u32_e32 v53, v53, v54
	v_cmp_gt_i32_e32 vcc, 0x100, v53
	v_cmp_eq_u32_e64 s[8:9], v53, v15
	s_nop 0
	v_cndmask_b32_e64 v55, 0, -1, vcc
	v_cndmask_b32_e32 v14, v14, v52, vcc
	v_bitop3_b32 v12, v12, v50, v55 bitop3:0xf8
	v_bitop3_b32 v13, v13, v51, v55 bitop3:0xf8
	v_bitop3_b32 v10, v10, v95, v55 bitop3:0x60
	v_bitop3_b32 v11, v11, v127, v55 bitop3:0x60
	s_cmp_lg_u64 s[8:9], 0
	s_cbranch_scc1 .Lmy_s2_h20
.Lmy_s2_p21:
	v_and_b32_e32 v50, v10, v96
	v_and_b32_e32 v51, v11, v128
	v_bcnt_u32_b32 v52, v50, v14
	v_bcnt_u32_b32 v52, v51, v52
	s_nop 1
	v_add_u32_dpp v53, v52, v52 quad_perm:[1,0,3,2] row_mask:0xf bank_mask:0xf bound_ctrl:1
	s_nop 1
	v_add_u32_dpp v53, v53, v53 quad_perm:[2,3,0,1] row_mask:0xf bank_mask:0xf bound_ctrl:1
	s_nop 1
	v_add_u32_dpp v53, v53, v53 row_half_mirror row_mask:0xf bank_mask:0xf bound_ctrl:1
	s_nop 1
	v_add_u32_dpp v53, v53, v53 row_mirror row_mask:0xf bank_mask:0xf bound_ctrl:1
	v_mov_b32_e32 v54, v53
	s_nop 1
	v_permlane16_swap_b32 v53, v54
	v_add_u32_e32 v53, v53, v54
	v_cmp_gt_i32_e32 vcc, 0x100, v53
	v_cmp_eq_u32_e64 s[8:9], v53, v15
	s_nop 0
	v_cndmask_b32_e64 v55, 0, -1, vcc
	v_cndmask_b32_e32 v14, v14, v52, vcc
	v_bitop3_b32 v12, v12, v50, v55 bitop3:0xf8
	v_bitop3_b32 v13, v13, v51, v55 bitop3:0xf8
	v_bitop3_b32 v10, v10, v96, v55 bitop3:0x60
	v_bitop3_b32 v11, v11, v128, v55 bitop3:0x60
	s_cmp_lg_u64 s[8:9], 0
	s_cbranch_scc1 .Lmy_s2_h21
.Lmy_s2_p22:
	v_and_b32_e32 v50, v10, v97
	v_and_b32_e32 v51, v11, v129
	v_bcnt_u32_b32 v52, v50, v14
	v_bcnt_u32_b32 v52, v51, v52
	s_nop 1
	v_add_u32_dpp v53, v52, v52 quad_perm:[1,0,3,2] row_mask:0xf bank_mask:0xf bound_ctrl:1
	s_nop 1
	v_add_u32_dpp v53, v53, v53 quad_perm:[2,3,0,1] row_mask:0xf bank_mask:0xf bound_ctrl:1
	s_nop 1
	v_add_u32_dpp v53, v53, v53 row_half_mirror row_mask:0xf bank_mask:0xf bound_ctrl:1
	s_nop 1
	v_add_u32_dpp v53, v53, v53 row_mirror row_mask:0xf bank_mask:0xf bound_ctrl:1
	v_mov_b32_e32 v54, v53
	s_nop 1
	v_permlane16_swap_b32 v53, v54
	v_add_u32_e32 v53, v53, v54
	v_cmp_gt_i32_e32 vcc, 0x100, v53
	v_cmp_eq_u32_e64 s[8:9], v53, v15
	s_nop 0
	v_cndmask_b32_e64 v55, 0, -1, vcc
	v_cndmask_b32_e32 v14, v14, v52, vcc
	v_bitop3_b32 v12, v12, v50, v55 bitop3:0xf8
	v_bitop3_b32 v13, v13, v51, v55 bitop3:0xf8
	v_bitop3_b32 v10, v10, v97, v55 bitop3:0x60
	v_bitop3_b32 v11, v11, v129, v55 bitop3:0x60
	s_cmp_lg_u64 s[8:9], 0
	s_cbranch_scc1 .Lmy_s2_h22
.Lmy_s2_p23:
	v_and_b32_e32 v50, v10, v98
	v_and_b32_e32 v51, v11, v130
	v_bcnt_u32_b32 v52, v50, v14
	v_bcnt_u32_b32 v52, v51, v52
	s_nop 1
	v_add_u32_dpp v53, v52, v52 quad_perm:[1,0,3,2] row_mask:0xf bank_mask:0xf bound_ctrl:1
	s_nop 1
	v_add_u32_dpp v53, v53, v53 quad_perm:[2,3,0,1] row_mask:0xf bank_mask:0xf bound_ctrl:1
	s_nop 1
	v_add_u32_dpp v53, v53, v53 row_half_mirror row_mask:0xf bank_mask:0xf bound_ctrl:1
	s_nop 1
	v_add_u32_dpp v53, v53, v53 row_mirror row_mask:0xf bank_mask:0xf bound_ctrl:1
	v_mov_b32_e32 v54, v53
	s_nop 1
	v_permlane16_swap_b32 v53, v54
	v_add_u32_e32 v53, v53, v54
	v_cmp_gt_i32_e32 vcc, 0x100, v53
	v_cmp_eq_u32_e64 s[8:9], v53, v15
	s_nop 0
	v_cndmask_b32_e64 v55, 0, -1, vcc
	v_cndmask_b32_e32 v14, v14, v52, vcc
	v_bitop3_b32 v12, v12, v50, v55 bitop3:0xf8
	v_bitop3_b32 v13, v13, v51, v55 bitop3:0xf8
	v_bitop3_b32 v10, v10, v98, v55 bitop3:0x60
	v_bitop3_b32 v11, v11, v130, v55 bitop3:0x60
	s_cmp_lg_u64 s[8:9], 0
	s_cbranch_scc1 .Lmy_s2_h23
.Lmy_s2_p24:
	v_and_b32_e32 v50, v10, v100
	v_and_b32_e32 v51, v11, v132
	v_bcnt_u32_b32 v52, v50, v14
	v_bcnt_u32_b32 v52, v51, v52
	s_nop 1
	v_add_u32_dpp v53, v52, v52 quad_perm:[1,0,3,2] row_mask:0xf bank_mask:0xf bound_ctrl:1
	s_nop 1
	v_add_u32_dpp v53, v53, v53 quad_perm:[2,3,0,1] row_mask:0xf bank_mask:0xf bound_ctrl:1
	s_nop 1
	v_add_u32_dpp v53, v53, v53 row_half_mirror row_mask:0xf bank_mask:0xf bound_ctrl:1
	s_nop 1
	v_add_u32_dpp v53, v53, v53 row_mirror row_mask:0xf bank_mask:0xf bound_ctrl:1
	v_mov_b32_e32 v54, v53
	s_nop 1
	v_permlane16_swap_b32 v53, v54
	v_add_u32_e32 v53, v53, v54
	v_cmp_gt_i32_e32 vcc, 0x100, v53
	v_cmp_eq_u32_e64 s[8:9], v53, v15
	s_nop 0
	v_cndmask_b32_e64 v55, 0, -1, vcc
	v_cndmask_b32_e32 v14, v14, v52, vcc
	v_bitop3_b32 v12, v12, v50, v55 bitop3:0xf8
	v_bitop3_b32 v13, v13, v51, v55 bitop3:0xf8
	v_bitop3_b32 v10, v10, v100, v55 bitop3:0x60
	v_bitop3_b32 v11, v11, v132, v55 bitop3:0x60
	s_cmp_lg_u64 s[8:9], 0
	s_cbranch_scc1 .Lmy_s2_h24
.Lmy_s2_p25:
	v_and_b32_e32 v50, v10, v101
	v_and_b32_e32 v51, v11, v133
	v_bcnt_u32_b32 v52, v50, v14
	v_bcnt_u32_b32 v52, v51, v52
	s_nop 1
	v_add_u32_dpp v53, v52, v52 quad_perm:[1,0,3,2] row_mask:0xf bank_mask:0xf bound_ctrl:1
	s_nop 1
	v_add_u32_dpp v53, v53, v53 quad_perm:[2,3,0,1] row_mask:0xf bank_mask:0xf bound_ctrl:1
	s_nop 1
	v_add_u32_dpp v53, v53, v53 row_half_mirror row_mask:0xf bank_mask:0xf bound_ctrl:1
	s_nop 1
	v_add_u32_dpp v53, v53, v53 row_mirror row_mask:0xf bank_mask:0xf bound_ctrl:1
	v_mov_b32_e32 v54, v53
	s_nop 1
	v_permlane16_swap_b32 v53, v54
	v_add_u32_e32 v53, v53, v54
	v_cmp_gt_i32_e32 vcc, 0x100, v53
	v_cmp_eq_u32_e64 s[8:9], v53, v15
	s_nop 0
	v_cndmask_b32_e64 v55, 0, -1, vcc
	v_cndmask_b32_e32 v14, v14, v52, vcc
	v_bitop3_b32 v12, v12, v50, v55 bitop3:0xf8
	v_bitop3_b32 v13, v13, v51, v55 bitop3:0xf8
	v_bitop3_b32 v10, v10, v101, v55 bitop3:0x60
	v_bitop3_b32 v11, v11, v133, v55 bitop3:0x60
	s_cmp_lg_u64 s[8:9], 0
	s_cbranch_scc1 .Lmy_s2_h25
.Lmy_s2_p26:
	v_and_b32_e32 v50, v10, v102
	v_and_b32_e32 v51, v11, v134
	v_bcnt_u32_b32 v52, v50, v14
	v_bcnt_u32_b32 v52, v51, v52
	s_nop 1
	v_add_u32_dpp v53, v52, v52 quad_perm:[1,0,3,2] row_mask:0xf bank_mask:0xf bound_ctrl:1
	s_nop 1
	v_add_u32_dpp v53, v53, v53 quad_perm:[2,3,0,1] row_mask:0xf bank_mask:0xf bound_ctrl:1
	s_nop 1
	v_add_u32_dpp v53, v53, v53 row_half_mirror row_mask:0xf bank_mask:0xf bound_ctrl:1
	s_nop 1
	v_add_u32_dpp v53, v53, v53 row_mirror row_mask:0xf bank_mask:0xf bound_ctrl:1
	v_mov_b32_e32 v54, v53
	s_nop 1
	v_permlane16_swap_b32 v53, v54
	v_add_u32_e32 v53, v53, v54
	v_cmp_gt_i32_e32 vcc, 0x100, v53
	v_cmp_eq_u32_e64 s[8:9], v53, v15
	s_nop 0
	v_cndmask_b32_e64 v55, 0, -1, vcc
	v_cndmask_b32_e32 v14, v14, v52, vcc
	v_bitop3_b32 v12, v12, v50, v55 bitop3:0xf8
	v_bitop3_b32 v13, v13, v51, v55 bitop3:0xf8
	v_bitop3_b32 v10, v10, v102, v55 bitop3:0x60
	v_bitop3_b32 v11, v11, v134, v55 bitop3:0x60
	s_cmp_lg_u64 s[8:9], 0
	s_cbranch_scc1 .Lmy_s2_h26
.Lmy_s2_p27:
	v_and_b32_e32 v50, v10, v103
	v_and_b32_e32 v51, v11, v135
	v_bcnt_u32_b32 v52, v50, v14
	v_bcnt_u32_b32 v52, v51, v52
	s_nop 1
	v_add_u32_dpp v53, v52, v52 quad_perm:[1,0,3,2] row_mask:0xf bank_mask:0xf bound_ctrl:1
	s_nop 1
	v_add_u32_dpp v53, v53, v53 quad_perm:[2,3,0,1] row_mask:0xf bank_mask:0xf bound_ctrl:1
	s_nop 1
	v_add_u32_dpp v53, v53, v53 row_half_mirror row_mask:0xf bank_mask:0xf bound_ctrl:1
	s_nop 1
	v_add_u32_dpp v53, v53, v53 row_mirror row_mask:0xf bank_mask:0xf bound_ctrl:1
	v_mov_b32_e32 v54, v53
	s_nop 1
	v_permlane16_swap_b32 v53, v54
	v_add_u32_e32 v53, v53, v54
	v_cmp_gt_i32_e32 vcc, 0x100, v53
	v_cmp_eq_u32_e64 s[8:9], v53, v15
	s_nop 0
	v_cndmask_b32_e64 v55, 0, -1, vcc
	v_cndmask_b32_e32 v14, v14, v52, vcc
	v_bitop3_b32 v12, v12, v50, v55 bitop3:0xf8
	v_bitop3_b32 v13, v13, v51, v55 bitop3:0xf8
	v_bitop3_b32 v10, v10, v103, v55 bitop3:0x60
	v_bitop3_b32 v11, v11, v135, v55 bitop3:0x60
	s_cmp_lg_u64 s[8:9], 0
	s_cbranch_scc1 .Lmy_s2_h27
.Lmy_s2_p28:
	v_and_b32_e32 v50, v10, v104
	v_and_b32_e32 v51, v11, v136
	v_bcnt_u32_b32 v52, v50, v14
	v_bcnt_u32_b32 v52, v51, v52
	s_nop 1
	v_add_u32_dpp v53, v52, v52 quad_perm:[1,0,3,2] row_mask:0xf bank_mask:0xf bound_ctrl:1
	s_nop 1
	v_add_u32_dpp v53, v53, v53 quad_perm:[2,3,0,1] row_mask:0xf bank_mask:0xf bound_ctrl:1
	s_nop 1
	v_add_u32_dpp v53, v53, v53 row_half_mirror row_mask:0xf bank_mask:0xf bound_ctrl:1
	s_nop 1
	v_add_u32_dpp v53, v53, v53 row_mirror row_mask:0xf bank_mask:0xf bound_ctrl:1
	v_mov_b32_e32 v54, v53
	s_nop 1
	v_permlane16_swap_b32 v53, v54
	v_add_u32_e32 v53, v53, v54
	v_cmp_gt_i32_e32 vcc, 0x100, v53
	v_cmp_eq_u32_e64 s[8:9], v53, v15
	s_nop 0
	v_cndmask_b32_e64 v55, 0, -1, vcc
	v_cndmask_b32_e32 v14, v14, v52, vcc
	v_bitop3_b32 v12, v12, v50, v55 bitop3:0xf8
	v_bitop3_b32 v13, v13, v51, v55 bitop3:0xf8
	v_bitop3_b32 v10, v10, v104, v55 bitop3:0x60
	v_bitop3_b32 v11, v11, v136, v55 bitop3:0x60
	s_cmp_lg_u64 s[8:9], 0
	s_cbranch_scc1 .Lmy_s2_h28
.Lmy_s2_p29:
	v_and_b32_e32 v50, v10, v105
	v_and_b32_e32 v51, v11, v137
	v_bcnt_u32_b32 v52, v50, v14
	v_bcnt_u32_b32 v52, v51, v52
	s_nop 1
	v_add_u32_dpp v53, v52, v52 quad_perm:[1,0,3,2] row_mask:0xf bank_mask:0xf bound_ctrl:1
	s_nop 1
	v_add_u32_dpp v53, v53, v53 quad_perm:[2,3,0,1] row_mask:0xf bank_mask:0xf bound_ctrl:1
	s_nop 1
	v_add_u32_dpp v53, v53, v53 row_half_mirror row_mask:0xf bank_mask:0xf bound_ctrl:1
	s_nop 1
	v_add_u32_dpp v53, v53, v53 row_mirror row_mask:0xf bank_mask:0xf bound_ctrl:1
	v_mov_b32_e32 v54, v53
	s_nop 1
	v_permlane16_swap_b32 v53, v54
	v_add_u32_e32 v53, v53, v54
	v_cmp_gt_i32_e32 vcc, 0x100, v53
	v_cmp_eq_u32_e64 s[8:9], v53, v15
	s_nop 0
	v_cndmask_b32_e64 v55, 0, -1, vcc
	v_cndmask_b32_e32 v14, v14, v52, vcc
	v_bitop3_b32 v12, v12, v50, v55 bitop3:0xf8
	v_bitop3_b32 v13, v13, v51, v55 bitop3:0xf8
	v_bitop3_b32 v10, v10, v105, v55 bitop3:0x60
	v_bitop3_b32 v11, v11, v137, v55 bitop3:0x60
	s_cmp_lg_u64 s[8:9], 0
	s_cbranch_scc1 .Lmy_s2_h29
.Lmy_s2_p30:
	v_and_b32_e32 v50, v10, v106
	v_and_b32_e32 v51, v11, v138
	v_bcnt_u32_b32 v52, v50, v14
	v_bcnt_u32_b32 v52, v51, v52
	s_nop 1
	v_add_u32_dpp v53, v52, v52 quad_perm:[1,0,3,2] row_mask:0xf bank_mask:0xf bound_ctrl:1
	s_nop 1
	v_add_u32_dpp v53, v53, v53 quad_perm:[2,3,0,1] row_mask:0xf bank_mask:0xf bound_ctrl:1
	s_nop 1
	v_add_u32_dpp v53, v53, v53 row_half_mirror row_mask:0xf bank_mask:0xf bound_ctrl:1
	s_nop 1
	v_add_u32_dpp v53, v53, v53 row_mirror row_mask:0xf bank_mask:0xf bound_ctrl:1
	v_mov_b32_e32 v54, v53
	s_nop 1
	v_permlane16_swap_b32 v53, v54
	v_add_u32_e32 v53, v53, v54
	v_cmp_gt_i32_e32 vcc, 0x100, v53
	v_cmp_eq_u32_e64 s[8:9], v53, v15
	s_nop 0
	v_cndmask_b32_e64 v55, 0, -1, vcc
	v_cndmask_b32_e32 v14, v14, v52, vcc
	v_bitop3_b32 v12, v12, v50, v55 bitop3:0xf8
	v_bitop3_b32 v13, v13, v51, v55 bitop3:0xf8
	v_bitop3_b32 v10, v10, v106, v55 bitop3:0x60
	v_bitop3_b32 v11, v11, v138, v55 bitop3:0x60
	s_cmp_lg_u64 s[8:9], 0
	s_cbranch_scc1 .Lmy_s2_h30
.Lmy_s2_p31:
	v_and_b32_e32 v50, v10, v107
	v_and_b32_e32 v51, v11, v139
	v_bcnt_u32_b32 v52, v50, v14
	v_bcnt_u32_b32 v52, v51, v52
	s_nop 1
	v_add_u32_dpp v53, v52, v52 quad_perm:[1,0,3,2] row_mask:0xf bank_mask:0xf bound_ctrl:1
	s_nop 1
	v_add_u32_dpp v53, v53, v53 quad_perm:[2,3,0,1] row_mask:0xf bank_mask:0xf bound_ctrl:1
	s_nop 1
	v_add_u32_dpp v53, v53, v53 row_half_mirror row_mask:0xf bank_mask:0xf bound_ctrl:1
	s_nop 1
	v_add_u32_dpp v53, v53, v53 row_mirror row_mask:0xf bank_mask:0xf bound_ctrl:1
	v_mov_b32_e32 v54, v53
	s_nop 1
	v_permlane16_swap_b32 v53, v54
	v_add_u32_e32 v53, v53, v54
	v_cmp_gt_i32_e32 vcc, 0x100, v53
	v_cmp_eq_u32_e64 s[8:9], v53, v15
	s_nop 0
	v_cndmask_b32_e64 v55, 0, -1, vcc
	v_cndmask_b32_e32 v14, v14, v52, vcc
	v_bitop3_b32 v12, v12, v50, v55 bitop3:0xf8
	v_bitop3_b32 v13, v13, v51, v55 bitop3:0xf8
	v_bitop3_b32 v10, v10, v107, v55 bitop3:0x60
	v_bitop3_b32 v11, v11, v139, v55 bitop3:0x60
	s_cmp_lg_u64 s[8:9], 0
	s_cbranch_scc1 .Lmy_s2_h31
.Lmy_s2_tie:
	s_nop 1
	v_add_u32_dpp v53, v14, v14 quad_perm:[1,0,3,2] row_mask:0xf bank_mask:0xf bound_ctrl:1
	s_nop 1
	v_add_u32_dpp v53, v53, v53 quad_perm:[2,3,0,1] row_mask:0xf bank_mask:0xf bound_ctrl:1
	s_nop 1
	v_add_u32_dpp v53, v53, v53 row_half_mirror row_mask:0xf bank_mask:0xf bound_ctrl:1
	s_nop 1
	v_add_u32_dpp v53, v53, v53 row_mirror row_mask:0xf bank_mask:0xf bound_ctrl:1
	v_mov_b32_e32 v54, v53
	s_nop 1
	v_permlane16_swap_b32 v53, v54
	v_add_u32_e32 v53, v53, v54
	v_sub_u32_e32 v16, 0x100, v53
	v_bcnt_u32_b32 v17, v10, 0
	v_bcnt_u32_b32 v18, v11, v17
	s_nop 1
	v_add_u32_dpp v19, v18, v18 row_shr:1 row_mask:0xf bank_mask:0xf bound_ctrl:1
	s_nop 1
	v_add_u32_dpp v19, v19, v19 row_shr:2 row_mask:0xf bank_mask:0xf bound_ctrl:1
	s_nop 1
	v_add_u32_dpp v19, v19, v19 row_shr:4 row_mask:0xf bank_mask:0xf bound_ctrl:1
	s_nop 1
	v_add_u32_dpp v19, v19, v19 row_shr:8 row_mask:0xf bank_mask:0xf bound_ctrl:1
	v_mov_b32_e32 v20, 0
	s_nop 1
	v_mov_b32_dpp v20, v19 row_bcast:15 row_mask:0xa bank_mask:0xf
	v_add_u32_e32 v19, v19, v20
	v_sub_u32_e32 v19, v19, v18
	v_sub_u32_e32 v21, v16, v19
	v_max_i32_e32 v21, 0, v21
	v_min_i32_e32 v21, v21, v18
	v_cndmask_b32_e64 v21, v21, 0, s[40:41]
	v_min_i32_e32 v22, v21, v17
	v_sub_u32_e32 v23, v21, v22
	v_mov_b32_e32 v24, 0
	v_mov_b32_e32 v25, 0
	s_mov_b64 s[44:45], exec

.Lmy_s2_tbe0:
	s_mov_b64 exec, s[44:45]
.Lmy_s2_tb1:
	v_cmp_lt_i32_e32 vcc, 0, v23
	s_and_b64 exec, exec, vcc
	s_cbranch_execz .Lmy_s2_tbe1
	v_ffbh_u32_e32 v26, v11
	v_lshrrev_b32_e64 v26, v26, s30
	v_or_b32_e32 v25, v25, v26
	v_xor_b32_e32 v11, v11, v26
	v_add_u32_e32 v23, -1, v23
	s_branch .Lmy_s2_tb1
.Lmy_s2_tbe1:
	s_mov_b64 exec, s[44:45]
	v_or_b32_e32 v24, v12, v24
	v_cndmask_b32_e64 v2, v24, v2, s[40:41]
	v_or_b32_e32 v25, v13, v25
	v_cndmask_b32_e64 v9, v25, v9, s[40:41]

.Lmy_s2_h0:
	s_andn2_b64 s[8:9], s[8:9], s[40:41]
	v_or_b32_e32 v56, v12, v10
	v_or_b32_e32 v57, v13, v11
	s_or_b64 s[40:41], s[40:41], s[8:9]
	v_cndmask_b32_e64 v2, v2, v56, s[8:9]
	v_cndmask_b32_e64 v9, v9, v57, s[8:9]
	s_cmp_eq_u64 s[40:41], -1
	s_cbranch_scc1 .Lmy_s2_done
	s_branch .Lmy_s2_p1

.LBB0_663:
	s_or_b64 exec, exec, s[6:7]
	s_mov_b32 s8, s18
	v_cmp_eq_u32_e32 vcc, 0, v0
	s_and_saveexec_b64 s[6:7], vcc
	s_cbranch_execnz .LBB0_772
	s_branch .LBB0_773
.LBB0_763:
	s_waitcnt lgkmcnt(0)
	v_bcnt_u32_b32 v3, v2, 0
	v_bcnt_u32_b32 v3, v9, v3
	v_mov_b32_e32 v11, v48
	s_lshr_b32 s6, s18, 5
	v_mov_b32_dpp v5, v3 row_shr:1 row_mask:0xf bank_mask:0xf bound_ctrl:1
	v_add_u32_e32 v4, v3, v5
	v_cmp_ne_u32_e32 vcc, 0, v2
	s_nop 0
	v_mov_b32_dpp v7, v4 row_shr:2 row_mask:0xf bank_mask:0xf bound_ctrl:1
	v_add_u32_e32 v4, v4, v7
	s_nop 1
	v_mov_b32_dpp v8, v4 row_shr:4 row_mask:0xf bank_mask:0xf bound_ctrl:1
	v_add_u32_e32 v4, v4, v8
	s_nop 1
	v_mov_b32_dpp v10, v4 row_shr:8 row_mask:0xf bank_mask:0xf bound_ctrl:1
	v_add_u32_e32 v4, v4, v10
	s_nop 1
	v_mov_b32_dpp v11, v4 row_bcast:15 row_mask:0xa bank_mask:0xf
	v_sub_u32_e32 v3, v11, v3
	v_add_u32_e32 v3, v3, v4
	v_mul_lo_u32 v4, v0, s6
	s_and_saveexec_b64 s[6:7], vcc
	s_cbranch_execz .LBB0_767
	v_add_u32_e32 v5, v11, v5
	v_lshlrev_b32_e32 v12, 9, v1
	v_add3_u32 v5, v5, v7, v8
	v_lshl_or_b32 v12, s4, 10, v12
	v_add_lshl_u32 v5, v5, v10, 1
	v_readlane_b32 s8, v255, 19
	s_nop 1
	v_add3_u32 v5, v12, v5, s8
	s_mov_b64 s[8:9], 0

.LBB0_911:
	ds_read_u16 v46, v45 offset:192
	s_waitcnt lgkmcnt(0)
	v_lshl_or_b32 v46, v46, 8, v246
	global_load_dwordx4 v[54:57], v46, s[50:51]
	global_load_dwordx4 v[58:61], v46, s[50:51] offset:64
	s_cmpk_lt_i32 s6, 0x71
	s_cbranch_scc0 .LBB0_782
	s_branch .LBB0_783
.LBB0_916:
	v_readlane_b32 s1, v255, 38
	s_mul_i32 s1, s1, 13
	v_readlane_b32 s92, v254, 3
	s_add_i32 s1, s1, 5
	v_readlane_b32 s93, v254, 4
	s_cmp_lt_i32 s1, s93
	v_readlane_b32 s56, v255, 24
	s_cselect_b64 s[4:5], -1, 0
	v_readlane_b32 s57, v255, 25
	s_and_b64 s[4:5], s[56:57], s[4:5]
	s_andn2_b64 vcc, exec, s[4:5]
	v_readlane_b32 s94, v254, 5
	v_readlane_b32 s95, v254, 6
	s_cbranch_vccnz .LBB0_928
	s_waitcnt vmcnt(0)
	v_readlane_b32 s4, v254, 9
	v_cmp_eq_u32_e32 vcc, 0, v234
	v_readlane_b32 s5, v254, 10
	s_and_b64 s[6:7], s[4:5], vcc
	s_barrier
	s_and_saveexec_b64 s[4:5], s[6:7]
	v_readlane_b32 s54, v255, 22
	v_readlane_b32 s88, v255, 26
	v_readlane_b32 s90, v255, 28
	v_readlane_b32 s55, v255, 23
	v_readlane_b32 s89, v255, 27
	v_readlane_b32 s91, v255, 29
	s_mov_b64 s[78:79], 0x800
	s_mov_b64 s[96:97], 0x50000
	v_readlane_b32 s26, v255, 41
	s_cbranch_execz .LBB0_966
	v_readlane_b32 s6, v254, 2
	s_waitcnt vmcnt(0) expcnt(0) lgkmcnt(0)
	s_nop 0
	v_mov_b32_e32 v0, s6
	ds_read_b32 v2, v0
	ds_read_b32 v0, v0 offset:4
	s_waitcnt lgkmcnt(1)
	v_cmp_ne_u32_e32 vcc, 0, v2
	s_cbranch_vccnz .LBB0_934
	v_readlane_b32 s8, v254, 0
	v_readlane_b32 s9, v254, 1
	s_load_dwordx2 s[6:7], s[8:9], 0x4
	s_mov_b32 s17, 1
	s_waitcnt lgkmcnt(0)
	s_mul_i32 s12, s6, s76
	s_mul_i32 s12, s12, s7
	s_branch .LBB0_921
